# hyena epilogue gate loads hoisted; expert-down epilogue token/weight loads batched; w_out epilogue residual loads prefetched many blocks ahead
# speedup vs baseline: 1.0269x; 1.0129x over previous
; #define LAS __attribute__((address_space(3)))
; #define HDSR(dst, addr, off) asm volatile("ds_read_b128 %0, %1 offset:%2" : "=v"(dst) : "v"(addr), "n"(off))
; #define HWAIT(a, b, c, d) asm volatile("s_waitcnt lgkmcnt(0)" : "+v"(a), "+v"(b), "+v"(c), "+v"(d))
; __device__ __forceinline__ void hyena_unit(KP Pk, Frame& F, int l, int cg) {
;     ...
;             const float bias = Pk->in[I_HBIAS][(l * 2 + o) * 512 + ch];
;             if (2 * F.wave < nblk / 4) {
;                 const int g0 = 2 * F.wave, dlo = 4 * g0 - nblk + 1, dhi = min(4 * g0 + 7, nblk - 1), nsteps = dhi - dlo + 1;
;                 const LAS unsigned char* ap = cop + ((-r32) & 7) * HY_CST + ((L - 32 * dlo - r32 + 8 * hi) & ~7) * 2;
;                 const LAS unsigned char* bp = Yin + (bb * YSTR + HY_PAD + 32 * (4 * g0 + ib - dlo) + 8 * hi) * 2;
;                 f32x16 acc0 = {}, acc1 = {};
;                 u32x2 gtv[4];
;                 { const bf16_t* gp = ZT + ((size_t)bb * 1536 + o * 512 + ch) * KEYS + pos0 + 32 * (4 * g0 + ib) + 4 * hi;
; #pragma unroll
;                   for (int q = 0; q < 4; ++q) gtv[q] = *(const u32x2*)(gp + 8 * q); }
;     ...
;                 bf16x8 R[6][2], A2[2][2];
;                 const unsigned apa = (unsigned)(uintptr_t)ap, bpa = (unsigned)(uintptr_t)bp;
;                 HDSR(R[2][0], bpa, 256); HDSR(R[2][1], bpa, 256 + 32); HDSR(R[3][0], bpa, 192); HDSR(R[3][1], bpa, 192 + 32);
;                 HDSR(R[4][0], bpa, 128); HDSR(R[4][1], bpa, 128 + 32); HDSR(R[5][0], bpa, 64); HDSR(R[5][1], bpa, 64 + 32);
;                 HDSR(R[0][0], bpa, 0); HDSR(R[0][1], bpa, 32); HDSR(A2[0][0], apa, 0); HDSR(A2[0][1], apa, 32);
;                 HWAIT(R[2][0], R[2][1], R[3][0], R[3][1]); HWAIT(R[4][0], R[4][1], R[5][0], R[5][1]); HWAIT(R[0][0], R[0][1], A2[0][0], A2[0][1]);
;     ...
;                 for (int gg = 0; gg < 2; ++gg) { const f32x16& acc = gg == 0 ? acc0 : acc1;
;                     const int t0 = 32 * (4 * (g0 + gg) + ib) + 4 * hi;
; #pragma unroll
;                     for (int q = 0; q < 4; ++q) { const u32x2 yo = *(const LAS u32x2*)(Yin + (bb * YSTR + HY_PAD + t0 + 8 * q) * 2); const u32x2 gt = gg == 0 ? gtv[q] : *(const u32x2*)(ZT + ((size_t)bb * 1536 + o * 512 + ch) * KEYS + pos0 + t0 + 8 * q);
.LBB0_714:
	s_andn2_b64 vcc, exec, s[42:43]
	s_waitcnt lgkmcnt(0)
	s_barrier
	s_cbranch_vccnz .LBB0_704
	s_and_b64 s[40:41], s[34:35], exec
	s_cselect_b32 s40, 0, 0x9c80
	s_lshl_b32 s60, s60, 9
	s_add_i32 s80, s19, s60
	s_ashr_i32 s81, s80, 31
	s_add_i32 s62, s40, 0
	s_lshl_b64 s[80:81], s[80:81], 2
	s_add_u32 s80, s26, s80
	s_addc_u32 s81, s27, s81
	v_lshl_add_u64 v[2:3], v[134:135], 0, s[60:61]
	global_load_dword v142, v0, s[80:81]
	v_mad_u64_u32 v[144:145], s[80:81], v2, s64, v[136:137]
	v_mad_i32_i24 v145, v3, s64, v145
	v_lshl_add_u64 v[2:3], v[126:127], 1, v[144:145]
	v_lshl_add_u64 v[2:3], v[124:125], 1, v[2:3]
	global_load_dwordx2 v[152:153], v[2:3], off
	global_load_dwordx2 v[150:151], v[2:3], off offset:16
	global_load_dwordx2 v[148:149], v[2:3], off offset:32
	global_load_dwordx2 v[146:147], v[2:3], off offset:48
	v_lshl_add_u64 v[196:197], v[130:131], 1, v[144:145]
	global_load_dwordx2 v[198:199], v[196:197], off
	global_load_dwordx2 v[200:201], v[196:197], off offset:16
	global_load_dwordx2 v[202:203], v[196:197], off offset:32
	global_load_dwordx2 v[204:205], v[196:197], off offset:48
	v_add3_u32 v1, s62, v167, v158
	ds_read_b128 v[72:75], v1 offset:0x100
	ds_read_b128 v[80:83], v1 offset:0x120
	ds_read_b128 v[76:79], v1 offset:0xc0
	ds_read_b128 v[88:91], v1 offset:0xe0
	ds_read_b128 v[84:87], v1 offset:0x80
	ds_read_b128 v[96:99], v1 offset:0xa0
	ds_read_b128 v[92:95], v1 offset:64
	ds_read_b128 v[104:107], v1 offset:0x60
	ds_read_b128 v[100:103], v1 offset:0
	ds_read_b128 v[112:115], v1 offset:32
	ds_read_b128 v[108:111], v168 offset:0
	ds_read_b128 v[116:119], v168 offset:32
	s_andn2_b64 vcc, exec, s[44:45]
	s_waitcnt lgkmcnt(0)
	s_waitcnt lgkmcnt(0)
	s_waitcnt lgkmcnt(0)
	s_cbranch_vccnz .LBB0_742
	v_mov_b32_e32 v14, v0
	v_mov_b32_e32 v15, v0
	v_mov_b32_e32 v1, v0
	v_mov_b32_e32 v2, v0
	v_mov_b32_e32 v3, v0
	v_mov_b32_e32 v4, v0
	v_mov_b32_e32 v5, v0
	v_mov_b32_e32 v6, v0
	v_mov_b32_e32 v7, v0
	v_mov_b32_e32 v8, v0
	v_mov_b32_e32 v9, v0
	v_mov_b32_e32 v10, v0
	v_mov_b32_e32 v11, v0
	v_mov_b32_e32 v12, v0
	v_mov_b32_e32 v13, v0
	v_mov_b64_e32 v[30:31], v[14:15]
	v_mov_b64_e32 v[46:47], v[14:15]
	v_add_u32_e32 v143, s40, v169
	s_mov_b32 s60, 0
	v_mov_b32_e32 v171, v170
	v_mov_b64_e32 v[28:29], v[12:13]
	v_mov_b64_e32 v[26:27], v[10:11]
	v_mov_b64_e32 v[24:25], v[8:9]
	v_mov_b64_e32 v[22:23], v[6:7]
	v_mov_b64_e32 v[20:21], v[4:5]
	v_mov_b64_e32 v[18:19], v[2:3]
	v_mov_b64_e32 v[16:17], v[0:1]
	v_mov_b64_e32 v[44:45], v[12:13]
	v_mov_b64_e32 v[42:43], v[10:11]
	v_mov_b64_e32 v[40:41], v[8:9]
	v_mov_b64_e32 v[38:39], v[6:7]
	v_mov_b64_e32 v[36:37], v[4:5]
	v_mov_b64_e32 v[34:35], v[2:3]
	v_mov_b64_e32 v[32:33], v[0:1]
	s_branch .LBB0_719

; #define LAS __attribute__((address_space(3)))
; __device__ __forceinline__ unsigned pk2(float lo, float hi) { return f2bf(lo) | (f2bf(hi) << 16); }
; __device__ __forceinline__ void hyena_unit(KP Pk, Frame& F, int l, int cg) {
;     ...
;                 for (int gg = 0; gg < 2; ++gg) { const f32x16& acc = gg == 0 ? acc0 : acc1;
;                     const int t0 = 32 * (4 * (g0 + gg) + ib) + 4 * hi;
; #pragma unroll
;                     for (int q = 0; q < 4; ++q) { const u32x2 yo = *(const LAS u32x2*)(Yin + (bb * YSTR + HY_PAD + t0 + 8 * q) * 2); const u32x2 gt = gg == 0 ? gtv[q] : *(const u32x2*)(ZT + ((size_t)bb * 1536 + o * 512 + ch) * KEYS + pos0 + t0 + 8 * q);
;                         const float v0 = bflo(gt.x) * (acc[4 * q + 0] + bflo(yo.x) * bias), v1 = bfhi(gt.x) * (acc[4 * q + 1] + bfhi(yo.x) * bias);
;                         const float v2 = bflo(gt.y) * (acc[4 * q + 2] + bflo(yo.y) * bias), v3 = bfhi(gt.y) * (acc[4 * q + 3] + bfhi(yo.y) * bias);
;                         u32x2 ov; ov.x = pk2(v0, v1); ov.y = pk2(v2, v3);
;                         if (o == 0) *(LAS u32x2*)(Yout + (bb * YSTR + HY_PAD + t0 + 8 * q) * 2) = ov;
;                         else *(u32x2*)(OT + ((size_t)bb * 512 + ch) * KEYS + pos0 + t0 + 8 * q) = ov; } }
.LBB0_743:
	v_add_u32_e32 v1, s62, v161
	ds_read_b64 v[2:3], v1
	s_nop 4
	v_mov_b32_e32 v8, v32
	v_mov_b32_e32 v9, v34
	s_waitcnt vmcnt(0)
	v_lshlrev_b32_e32 v5, 16, v153
	v_lshlrev_b32_e32 v4, 16, v152
	s_waitcnt lgkmcnt(0)
	v_lshlrev_b32_e32 v7, 16, v3
	v_lshlrev_b32_e32 v6, 16, v2
	v_pk_fma_f32 v[6:7], v[142:143], v[6:7], v[8:9] op_sel_hi:[0,1,1]
	v_and_b32_e32 v3, 0xffff0000, v3
	v_and_b32_e32 v2, 0xffff0000, v2
	v_mov_b32_e32 v34, v33
	v_pk_mul_f32 v[4:5], v[6:7], v[4:5]
	v_and_b32_e32 v7, 0xffff0000, v153
	v_and_b32_e32 v6, 0xffff0000, v152
	v_pk_fma_f32 v[2:3], v[142:143], v[2:3], v[34:35] op_sel_hi:[0,1,1]
	v_pk_mul_f32 v[2:3], v[2:3], v[6:7]
	v_and_b32_sdwa v6, v5, v227 dst_sel:DWORD dst_unused:UNUSED_PAD src0_sel:WORD_1 src1_sel:DWORD
	v_and_b32_sdwa v7, v4, v227 dst_sel:DWORD dst_unused:UNUSED_PAD src0_sel:WORD_1 src1_sel:DWORD
	v_add3_u32 v4, v4, v7, s23
	v_add3_u32 v5, v5, v6, s23
	v_and_b32_sdwa v6, v3, v227 dst_sel:DWORD dst_unused:UNUSED_PAD src0_sel:WORD_1 src1_sel:DWORD
	v_and_b32_sdwa v7, v2, v227 dst_sel:DWORD dst_unused:UNUSED_PAD src0_sel:WORD_1 src1_sel:DWORD
	v_add3_u32 v3, v3, v6, s23
	v_add3_u32 v2, v2, v7, s23
	s_and_b64 s[34:35], s[34:35], exec
	v_and_b32_e32 v3, 0xffff0000, v3
	v_and_b32_e32 v2, 0xffff0000, v2
	s_cselect_b32 s40, 0x9c80, 0
	v_or_b32_sdwa v3, v3, v5 dst_sel:DWORD dst_unused:UNUSED_PAD src0_sel:DWORD src1_sel:WORD_1
	v_or_b32_sdwa v2, v2, v4 dst_sel:DWORD dst_unused:UNUSED_PAD src0_sel:DWORD src1_sel:WORD_1
	s_mov_b64 s[34:35], -1
	s_and_b64 vcc, exec, s[46:47]
	s_cbranch_vccz .LBB0_745
	global_store_dwordx2 v[138:139], v[2:3], off
	s_mov_b64 s[34:35], 0

; #define LAS __attribute__((address_space(3)))
; __device__ __forceinline__ unsigned pk2(float lo, float hi) { return f2bf(lo) | (f2bf(hi) << 16); }
; __device__ __forceinline__ void hyena_unit(KP Pk, Frame& F, int l, int cg) {
;     ...
;                 for (int gg = 0; gg < 2; ++gg) { const f32x16& acc = gg == 0 ? acc0 : acc1;
;                     const int t0 = 32 * (4 * (g0 + gg) + ib) + 4 * hi;
; #pragma unroll
;                     for (int q = 0; q < 4; ++q) { const u32x2 yo = *(const LAS u32x2*)(Yin + (bb * YSTR + HY_PAD + t0 + 8 * q) * 2); const u32x2 gt = gg == 0 ? gtv[q] : *(const u32x2*)(ZT + ((size_t)bb * 1536 + o * 512 + ch) * KEYS + pos0 + t0 + 8 * q);
;                         const float v0 = bflo(gt.x) * (acc[4 * q + 0] + bflo(yo.x) * bias), v1 = bfhi(gt.x) * (acc[4 * q + 1] + bfhi(yo.x) * bias);
;                         const float v2 = bflo(gt.y) * (acc[4 * q + 2] + bflo(yo.y) * bias), v3 = bfhi(gt.y) * (acc[4 * q + 3] + bfhi(yo.y) * bias);
;                         u32x2 ov; ov.x = pk2(v0, v1); ov.y = pk2(v2, v3);
;                         if (o == 0) *(LAS u32x2*)(Yout + (bb * YSTR + HY_PAD + t0 + 8 * q) * 2) = ov;
;                         else *(u32x2*)(OT + ((size_t)bb * 512 + ch) * KEYS + pos0 + t0 + 8 * q) = ov; } }
.LBB0_747:
	ds_read_b64 v[2:3], v1 offset:16
	v_mov_b32_e32 v143, v142
	v_mov_b32_e32 v10, v36
	v_mov_b32_e32 v11, v38
	v_lshlrev_b32_e32 v7, 16, v151
	s_waitcnt lgkmcnt(0)
	v_lshlrev_b32_e32 v9, 16, v3
	v_lshlrev_b32_e32 v8, 16, v2
	v_lshlrev_b32_e32 v6, 16, v150
	v_pk_fma_f32 v[8:9], v[142:143], v[8:9], v[10:11]
	v_and_b32_e32 v3, 0xffff0000, v3
	v_and_b32_e32 v2, 0xffff0000, v2
	v_mov_b32_e32 v38, v37
	v_pk_mul_f32 v[6:7], v[8:9], v[6:7]
	v_and_b32_e32 v9, 0xffff0000, v151
	v_and_b32_e32 v8, 0xffff0000, v150
	v_pk_fma_f32 v[2:3], v[142:143], v[2:3], v[38:39]
	v_and_b32_sdwa v5, v7, v227 dst_sel:DWORD dst_unused:UNUSED_PAD src0_sel:WORD_1 src1_sel:DWORD
	v_pk_mul_f32 v[2:3], v[2:3], v[8:9]
	v_and_b32_sdwa v8, v6, v227 dst_sel:DWORD dst_unused:UNUSED_PAD src0_sel:WORD_1 src1_sel:DWORD
	v_add3_u32 v5, v7, v5, s23
	v_and_b32_sdwa v7, v3, v227 dst_sel:DWORD dst_unused:UNUSED_PAD src0_sel:WORD_1 src1_sel:DWORD
	v_add3_u32 v6, v6, v8, s23
	v_and_b32_sdwa v8, v2, v227 dst_sel:DWORD dst_unused:UNUSED_PAD src0_sel:WORD_1 src1_sel:DWORD
	v_add3_u32 v3, v3, v7, s23
	v_add3_u32 v2, v2, v8, s23
	v_and_b32_e32 v3, 0xffff0000, v3
	v_and_b32_e32 v2, 0xffff0000, v2
	v_or_b32_sdwa v3, v3, v5 dst_sel:DWORD dst_unused:UNUSED_PAD src0_sel:DWORD src1_sel:WORD_1
	v_cndmask_b32_e64 v5, 0, 1, s[46:47]
	v_or_b32_sdwa v2, v2, v6 dst_sel:DWORD dst_unused:UNUSED_PAD src0_sel:DWORD src1_sel:WORD_1
	v_cmp_ne_u32_e64 s[40:41], 1, v5
	s_andn2_b64 vcc, exec, s[46:47]
	s_mov_b64 s[34:35], -1
	s_cbranch_vccnz .LBB0_749
	s_mov_b64 s[34:35], 0
	global_store_dwordx2 v[138:139], v[2:3], off offset:16

; #define LAS __attribute__((address_space(3)))
; __device__ __forceinline__ unsigned pk2(float lo, float hi) { return f2bf(lo) | (f2bf(hi) << 16); }
; __device__ __forceinline__ void hyena_unit(KP Pk, Frame& F, int l, int cg) {
;     ...
;                 for (int gg = 0; gg < 2; ++gg) { const f32x16& acc = gg == 0 ? acc0 : acc1;
;                     const int t0 = 32 * (4 * (g0 + gg) + ib) + 4 * hi;
; #pragma unroll
;                     for (int q = 0; q < 4; ++q) { const u32x2 yo = *(const LAS u32x2*)(Yin + (bb * YSTR + HY_PAD + t0 + 8 * q) * 2); const u32x2 gt = gg == 0 ? gtv[q] : *(const u32x2*)(ZT + ((size_t)bb * 1536 + o * 512 + ch) * KEYS + pos0 + t0 + 8 * q);
;                         const float v0 = bflo(gt.x) * (acc[4 * q + 0] + bflo(yo.x) * bias), v1 = bfhi(gt.x) * (acc[4 * q + 1] + bfhi(yo.x) * bias);
;                         const float v2 = bflo(gt.y) * (acc[4 * q + 2] + bflo(yo.y) * bias), v3 = bfhi(gt.y) * (acc[4 * q + 3] + bfhi(yo.y) * bias);
;                         u32x2 ov; ov.x = pk2(v0, v1); ov.y = pk2(v2, v3);
;                         if (o == 0) *(LAS u32x2*)(Yout + (bb * YSTR + HY_PAD + t0 + 8 * q) * 2) = ov;
;                         else *(u32x2*)(OT + ((size_t)bb * 512 + ch) * KEYS + pos0 + t0 + 8 * q) = ov; } }
.LBB0_751:
	ds_read_b64 v[2:3], v1 offset:32
	v_mov_b32_e32 v8, v40
	v_mov_b32_e32 v9, v42
	v_lshlrev_b32_e32 v7, 16, v149
	v_lshlrev_b32_e32 v6, 16, v148
	s_waitcnt lgkmcnt(0)
	v_lshlrev_b32_e32 v11, 16, v3
	v_lshlrev_b32_e32 v10, 16, v2
	v_pk_fma_f32 v[8:9], v[142:143], v[10:11], v[8:9]
	v_and_b32_e32 v3, 0xffff0000, v3
	v_and_b32_e32 v2, 0xffff0000, v2
	v_mov_b32_e32 v42, v41
	v_pk_mul_f32 v[6:7], v[8:9], v[6:7]
	v_and_b32_e32 v9, 0xffff0000, v149
	v_and_b32_e32 v8, 0xffff0000, v148
	v_pk_fma_f32 v[2:3], v[142:143], v[2:3], v[42:43]
	v_and_b32_sdwa v5, v7, v227 dst_sel:DWORD dst_unused:UNUSED_PAD src0_sel:WORD_1 src1_sel:DWORD
	v_pk_mul_f32 v[2:3], v[2:3], v[8:9]
	v_and_b32_sdwa v8, v6, v227 dst_sel:DWORD dst_unused:UNUSED_PAD src0_sel:WORD_1 src1_sel:DWORD
	v_add3_u32 v6, v6, v8, s23
	v_add3_u32 v5, v7, v5, s23
	v_and_b32_sdwa v7, v3, v227 dst_sel:DWORD dst_unused:UNUSED_PAD src0_sel:WORD_1 src1_sel:DWORD
	v_and_b32_sdwa v8, v2, v227 dst_sel:DWORD dst_unused:UNUSED_PAD src0_sel:WORD_1 src1_sel:DWORD
	v_add3_u32 v3, v3, v7, s23
	v_add3_u32 v2, v2, v8, s23
	v_and_b32_e32 v3, 0xffff0000, v3
	v_and_b32_e32 v2, 0xffff0000, v2
	v_or_b32_sdwa v3, v3, v5 dst_sel:DWORD dst_unused:UNUSED_PAD src0_sel:DWORD src1_sel:WORD_1
	v_or_b32_sdwa v2, v2, v6 dst_sel:DWORD dst_unused:UNUSED_PAD src0_sel:DWORD src1_sel:WORD_1
	s_and_b64 vcc, exec, s[40:41]
	s_mov_b64 s[34:35], -1
	s_cbranch_vccnz .LBB0_753
	s_mov_b64 s[34:35], 0
	global_store_dwordx2 v[138:139], v[2:3], off offset:32

; #define LAS __attribute__((address_space(3)))
; __device__ __forceinline__ unsigned pk2(float lo, float hi) { return f2bf(lo) | (f2bf(hi) << 16); }
; __device__ __forceinline__ void hyena_unit(KP Pk, Frame& F, int l, int cg) {
;     ...
;                 for (int gg = 0; gg < 2; ++gg) { const f32x16& acc = gg == 0 ? acc0 : acc1;
;                     const int t0 = 32 * (4 * (g0 + gg) + ib) + 4 * hi;
; #pragma unroll
;                     for (int q = 0; q < 4; ++q) { const u32x2 yo = *(const LAS u32x2*)(Yin + (bb * YSTR + HY_PAD + t0 + 8 * q) * 2); const u32x2 gt = gg == 0 ? gtv[q] : *(const u32x2*)(ZT + ((size_t)bb * 1536 + o * 512 + ch) * KEYS + pos0 + t0 + 8 * q);
;                         const float v0 = bflo(gt.x) * (acc[4 * q + 0] + bflo(yo.x) * bias), v1 = bfhi(gt.x) * (acc[4 * q + 1] + bfhi(yo.x) * bias);
;                         const float v2 = bflo(gt.y) * (acc[4 * q + 2] + bflo(yo.y) * bias), v3 = bfhi(gt.y) * (acc[4 * q + 3] + bfhi(yo.y) * bias);
;                         u32x2 ov; ov.x = pk2(v0, v1); ov.y = pk2(v2, v3);
;                         if (o == 0) *(LAS u32x2*)(Yout + (bb * YSTR + HY_PAD + t0 + 8 * q) * 2) = ov;
;                         else *(u32x2*)(OT + ((size_t)bb * 512 + ch) * KEYS + pos0 + t0 + 8 * q) = ov; } }
.LBB0_755:
	ds_read_b64 v[2:3], v1 offset:48
	v_mov_b32_e32 v8, v44
	v_mov_b32_e32 v9, v46
	v_lshlrev_b32_e32 v7, 16, v147
	v_lshlrev_b32_e32 v6, 16, v146
	s_waitcnt lgkmcnt(0)
	v_lshlrev_b32_e32 v11, 16, v3
	v_lshlrev_b32_e32 v10, 16, v2
	v_pk_fma_f32 v[8:9], v[142:143], v[10:11], v[8:9]
	v_and_b32_e32 v3, 0xffff0000, v3
	v_and_b32_e32 v2, 0xffff0000, v2
	v_mov_b32_e32 v46, v45
	v_pk_mul_f32 v[6:7], v[8:9], v[6:7]
	v_and_b32_e32 v9, 0xffff0000, v147
	v_and_b32_e32 v8, 0xffff0000, v146
	v_pk_fma_f32 v[2:3], v[142:143], v[2:3], v[46:47]
	v_and_b32_sdwa v1, v7, v227 dst_sel:DWORD dst_unused:UNUSED_PAD src0_sel:WORD_1 src1_sel:DWORD
	v_pk_mul_f32 v[2:3], v[2:3], v[8:9]
	v_and_b32_sdwa v5, v6, v227 dst_sel:DWORD dst_unused:UNUSED_PAD src0_sel:WORD_1 src1_sel:DWORD
	v_add3_u32 v5, v6, v5, s23
	v_add3_u32 v1, v7, v1, s23
	v_and_b32_sdwa v6, v3, v227 dst_sel:DWORD dst_unused:UNUSED_PAD src0_sel:WORD_1 src1_sel:DWORD
	v_and_b32_sdwa v7, v2, v227 dst_sel:DWORD dst_unused:UNUSED_PAD src0_sel:WORD_1 src1_sel:DWORD
	v_add3_u32 v3, v3, v6, s23
	v_add3_u32 v2, v2, v7, s23
	v_and_b32_e32 v3, 0xffff0000, v3
	v_and_b32_e32 v2, 0xffff0000, v2
	v_or_b32_sdwa v3, v3, v1 dst_sel:DWORD dst_unused:UNUSED_PAD src0_sel:DWORD src1_sel:WORD_1
	v_or_b32_sdwa v2, v2, v5 dst_sel:DWORD dst_unused:UNUSED_PAD src0_sel:DWORD src1_sel:WORD_1
	s_and_b64 vcc, exec, s[40:41]
	s_mov_b64 s[34:35], -1
	s_cbranch_vccnz .LBB0_757
	s_mov_b64 s[34:35], 0
	global_store_dwordx2 v[138:139], v[2:3], off offset:48

; #define LAS __attribute__((address_space(3)))
; __device__ __forceinline__ unsigned pk2(float lo, float hi) { return f2bf(lo) | (f2bf(hi) << 16); }
; __device__ __forceinline__ void hyena_unit(KP Pk, Frame& F, int l, int cg) {
;     ...
;                 for (int gg = 0; gg < 2; ++gg) { const f32x16& acc = gg == 0 ? acc0 : acc1;
;                     const int t0 = 32 * (4 * (g0 + gg) + ib) + 4 * hi;
; #pragma unroll
;                     for (int q = 0; q < 4; ++q) { const u32x2 yo = *(const LAS u32x2*)(Yin + (bb * YSTR + HY_PAD + t0 + 8 * q) * 2); const u32x2 gt = gg == 0 ? gtv[q] : *(const u32x2*)(ZT + ((size_t)bb * 1536 + o * 512 + ch) * KEYS + pos0 + t0 + 8 * q);
;                         const float v0 = bflo(gt.x) * (acc[4 * q + 0] + bflo(yo.x) * bias), v1 = bfhi(gt.x) * (acc[4 * q + 1] + bfhi(yo.x) * bias);
;                         const float v2 = bflo(gt.y) * (acc[4 * q + 2] + bflo(yo.y) * bias), v3 = bfhi(gt.y) * (acc[4 * q + 3] + bfhi(yo.y) * bias);
;                         u32x2 ov; ov.x = pk2(v0, v1); ov.y = pk2(v2, v3);
;                         if (o == 0) *(LAS u32x2*)(Yout + (bb * YSTR + HY_PAD + t0 + 8 * q) * 2) = ov;
;                         else *(u32x2*)(OT + ((size_t)bb * 512 + ch) * KEYS + pos0 + t0 + 8 * q) = ov; } }
.LBB0_759:
	v_add_u32_e32 v6, s62, v162
	ds_read_b64 v[8:9], v6
	v_mov_b32_e32 v10, v16
	v_mov_b32_e32 v11, v18
	v_mov_b32_e32 v18, v17
	s_and_b64 vcc, exec, s[40:41]
	s_waitcnt lgkmcnt(0)
	v_lshlrev_b32_e32 v13, 16, v9
	v_lshlrev_b32_e32 v12, 16, v8
	v_and_b32_e32 v9, 0xffff0000, v9
	v_and_b32_e32 v8, 0xffff0000, v8
	v_pk_fma_f32 v[10:11], v[142:143], v[12:13], v[10:11]
	v_pk_fma_f32 v[8:9], v[142:143], v[8:9], v[18:19]
	s_mov_b64 s[34:35], -1
	v_lshlrev_b32_e32 v13, 16, v199
	v_lshlrev_b32_e32 v12, 16, v198
	v_and_b32_e32 v5, 0xffff0000, v199
	v_and_b32_e32 v4, 0xffff0000, v198
	v_pk_mul_f32 v[4:5], v[8:9], v[4:5]
	v_pk_mul_f32 v[10:11], v[10:11], v[12:13]
	v_and_b32_sdwa v8, v5, v227 dst_sel:DWORD dst_unused:UNUSED_PAD src0_sel:WORD_1 src1_sel:DWORD
	v_and_b32_sdwa v9, v4, v227 dst_sel:DWORD dst_unused:UNUSED_PAD src0_sel:WORD_1 src1_sel:DWORD
	v_and_b32_sdwa v1, v11, v227 dst_sel:DWORD dst_unused:UNUSED_PAD src0_sel:WORD_1 src1_sel:DWORD
	v_and_b32_sdwa v7, v10, v227 dst_sel:DWORD dst_unused:UNUSED_PAD src0_sel:WORD_1 src1_sel:DWORD
	v_add3_u32 v5, v5, v8, s23
	v_add3_u32 v4, v4, v9, s23
	v_add3_u32 v7, v10, v7, s23
	v_add3_u32 v1, v11, v1, s23
	v_and_b32_e32 v5, 0xffff0000, v5
	v_and_b32_e32 v4, 0xffff0000, v4
	v_or_b32_sdwa v5, v5, v1 dst_sel:DWORD dst_unused:UNUSED_PAD src0_sel:DWORD src1_sel:WORD_1
	v_or_b32_sdwa v4, v4, v7 dst_sel:DWORD dst_unused:UNUSED_PAD src0_sel:DWORD src1_sel:WORD_1
	s_cbranch_vccnz .LBB0_761
	s_mov_b64 s[34:35], 0
	global_store_dwordx2 v[140:141], v[4:5], off

; #define LAS __attribute__((address_space(3)))
; __device__ __forceinline__ unsigned pk2(float lo, float hi) { return f2bf(lo) | (f2bf(hi) << 16); }
; __device__ __forceinline__ void hyena_unit(KP Pk, Frame& F, int l, int cg) {
;     ...
;                 for (int gg = 0; gg < 2; ++gg) { const f32x16& acc = gg == 0 ? acc0 : acc1;
;                     const int t0 = 32 * (4 * (g0 + gg) + ib) + 4 * hi;
; #pragma unroll
;                     for (int q = 0; q < 4; ++q) { const u32x2 yo = *(const LAS u32x2*)(Yin + (bb * YSTR + HY_PAD + t0 + 8 * q) * 2); const u32x2 gt = gg == 0 ? gtv[q] : *(const u32x2*)(ZT + ((size_t)bb * 1536 + o * 512 + ch) * KEYS + pos0 + t0 + 8 * q);
;                         const float v0 = bflo(gt.x) * (acc[4 * q + 0] + bflo(yo.x) * bias), v1 = bfhi(gt.x) * (acc[4 * q + 1] + bfhi(yo.x) * bias);
;                         const float v2 = bflo(gt.y) * (acc[4 * q + 2] + bflo(yo.y) * bias), v3 = bfhi(gt.y) * (acc[4 * q + 3] + bfhi(yo.y) * bias);
;                         u32x2 ov; ov.x = pk2(v0, v1); ov.y = pk2(v2, v3);
;                         if (o == 0) *(LAS u32x2*)(Yout + (bb * YSTR + HY_PAD + t0 + 8 * q) * 2) = ov;
;                         else *(u32x2*)(OT + ((size_t)bb * 512 + ch) * KEYS + pos0 + t0 + 8 * q) = ov; } }
.LBB0_763:
	ds_read_b64 v[8:9], v6 offset:16
	v_mov_b32_e32 v10, v20
	v_mov_b32_e32 v11, v22
	v_mov_b32_e32 v22, v21
	s_and_b64 vcc, exec, s[40:41]
	s_waitcnt lgkmcnt(0)
	v_lshlrev_b32_e32 v13, 16, v9
	v_lshlrev_b32_e32 v12, 16, v8
	v_and_b32_e32 v9, 0xffff0000, v9
	v_and_b32_e32 v8, 0xffff0000, v8
	v_pk_fma_f32 v[10:11], v[142:143], v[12:13], v[10:11]
	v_pk_fma_f32 v[8:9], v[142:143], v[8:9], v[22:23]
	s_mov_b64 s[34:35], -1
	v_lshlrev_b32_e32 v13, 16, v201
	v_lshlrev_b32_e32 v12, 16, v200
	v_and_b32_e32 v5, 0xffff0000, v201
	v_and_b32_e32 v4, 0xffff0000, v200
	v_pk_mul_f32 v[4:5], v[8:9], v[4:5]
	v_pk_mul_f32 v[10:11], v[10:11], v[12:13]
	v_and_b32_sdwa v9, v5, v227 dst_sel:DWORD dst_unused:UNUSED_PAD src0_sel:WORD_1 src1_sel:DWORD
	v_and_b32_sdwa v12, v4, v227 dst_sel:DWORD dst_unused:UNUSED_PAD src0_sel:WORD_1 src1_sel:DWORD
	v_and_b32_sdwa v7, v11, v227 dst_sel:DWORD dst_unused:UNUSED_PAD src0_sel:WORD_1 src1_sel:DWORD
	v_and_b32_sdwa v8, v10, v227 dst_sel:DWORD dst_unused:UNUSED_PAD src0_sel:WORD_1 src1_sel:DWORD
	v_add3_u32 v5, v5, v9, s23
	v_add3_u32 v4, v4, v12, s23
	v_add3_u32 v8, v10, v8, s23
	v_add3_u32 v7, v11, v7, s23
	v_and_b32_e32 v5, 0xffff0000, v5
	v_and_b32_e32 v4, 0xffff0000, v4
	v_or_b32_sdwa v5, v5, v7 dst_sel:DWORD dst_unused:UNUSED_PAD src0_sel:DWORD src1_sel:WORD_1
	v_or_b32_sdwa v4, v4, v8 dst_sel:DWORD dst_unused:UNUSED_PAD src0_sel:DWORD src1_sel:WORD_1
	s_cbranch_vccnz .LBB0_765
	s_mov_b64 s[34:35], 0
	global_store_dwordx2 v[140:141], v[4:5], off offset:16

; #define LAS __attribute__((address_space(3)))
; __device__ __forceinline__ unsigned pk2(float lo, float hi) { return f2bf(lo) | (f2bf(hi) << 16); }
; __device__ __forceinline__ void hyena_unit(KP Pk, Frame& F, int l, int cg) {
;     ...
;                 for (int gg = 0; gg < 2; ++gg) { const f32x16& acc = gg == 0 ? acc0 : acc1;
;                     const int t0 = 32 * (4 * (g0 + gg) + ib) + 4 * hi;
; #pragma unroll
;                     for (int q = 0; q < 4; ++q) { const u32x2 yo = *(const LAS u32x2*)(Yin + (bb * YSTR + HY_PAD + t0 + 8 * q) * 2); const u32x2 gt = gg == 0 ? gtv[q] : *(const u32x2*)(ZT + ((size_t)bb * 1536 + o * 512 + ch) * KEYS + pos0 + t0 + 8 * q);
;                         const float v0 = bflo(gt.x) * (acc[4 * q + 0] + bflo(yo.x) * bias), v1 = bfhi(gt.x) * (acc[4 * q + 1] + bfhi(yo.x) * bias);
;                         const float v2 = bflo(gt.y) * (acc[4 * q + 2] + bflo(yo.y) * bias), v3 = bfhi(gt.y) * (acc[4 * q + 3] + bfhi(yo.y) * bias);
;                         u32x2 ov; ov.x = pk2(v0, v1); ov.y = pk2(v2, v3);
;                         if (o == 0) *(LAS u32x2*)(Yout + (bb * YSTR + HY_PAD + t0 + 8 * q) * 2) = ov;
;                         else *(u32x2*)(OT + ((size_t)bb * 512 + ch) * KEYS + pos0 + t0 + 8 * q) = ov; } }
.LBB0_767:
	ds_read_b64 v[8:9], v6 offset:32
	v_mov_b32_e32 v10, v24
	v_mov_b32_e32 v11, v26
	v_mov_b32_e32 v26, v25
	s_and_b64 vcc, exec, s[40:41]
	s_waitcnt lgkmcnt(0)
	v_lshlrev_b32_e32 v13, 16, v9
	v_lshlrev_b32_e32 v12, 16, v8
	v_and_b32_e32 v9, 0xffff0000, v9
	v_and_b32_e32 v8, 0xffff0000, v8
	v_pk_fma_f32 v[10:11], v[142:143], v[12:13], v[10:11]
	v_pk_fma_f32 v[8:9], v[142:143], v[8:9], v[26:27]
	s_mov_b64 s[34:35], -1
	v_lshlrev_b32_e32 v13, 16, v203
	v_lshlrev_b32_e32 v12, 16, v202
	v_and_b32_e32 v5, 0xffff0000, v203
	v_and_b32_e32 v4, 0xffff0000, v202
	v_pk_mul_f32 v[4:5], v[8:9], v[4:5]
	v_pk_mul_f32 v[10:11], v[10:11], v[12:13]
	v_and_b32_sdwa v9, v5, v227 dst_sel:DWORD dst_unused:UNUSED_PAD src0_sel:WORD_1 src1_sel:DWORD
	v_and_b32_sdwa v12, v4, v227 dst_sel:DWORD dst_unused:UNUSED_PAD src0_sel:WORD_1 src1_sel:DWORD
	v_and_b32_sdwa v7, v11, v227 dst_sel:DWORD dst_unused:UNUSED_PAD src0_sel:WORD_1 src1_sel:DWORD
	v_and_b32_sdwa v8, v10, v227 dst_sel:DWORD dst_unused:UNUSED_PAD src0_sel:WORD_1 src1_sel:DWORD
	v_add3_u32 v5, v5, v9, s23
	v_add3_u32 v4, v4, v12, s23
	v_add3_u32 v8, v10, v8, s23
	v_add3_u32 v7, v11, v7, s23
	v_and_b32_e32 v5, 0xffff0000, v5
	v_and_b32_e32 v4, 0xffff0000, v4
	v_or_b32_sdwa v5, v5, v7 dst_sel:DWORD dst_unused:UNUSED_PAD src0_sel:DWORD src1_sel:WORD_1
	v_or_b32_sdwa v4, v4, v8 dst_sel:DWORD dst_unused:UNUSED_PAD src0_sel:DWORD src1_sel:WORD_1
	s_cbranch_vccnz .LBB0_769
	s_mov_b64 s[34:35], 0
	global_store_dwordx2 v[140:141], v[4:5], off offset:32

; #define LAS __attribute__((address_space(3)))
; __device__ __forceinline__ unsigned pk2(float lo, float hi) { return f2bf(lo) | (f2bf(hi) << 16); }
; __device__ __forceinline__ void hyena_unit(KP Pk, Frame& F, int l, int cg) {
;     ...
;                 for (int gg = 0; gg < 2; ++gg) { const f32x16& acc = gg == 0 ? acc0 : acc1;
;                     const int t0 = 32 * (4 * (g0 + gg) + ib) + 4 * hi;
; #pragma unroll
;                     for (int q = 0; q < 4; ++q) { const u32x2 yo = *(const LAS u32x2*)(Yin + (bb * YSTR + HY_PAD + t0 + 8 * q) * 2); const u32x2 gt = gg == 0 ? gtv[q] : *(const u32x2*)(ZT + ((size_t)bb * 1536 + o * 512 + ch) * KEYS + pos0 + t0 + 8 * q);
;                         const float v0 = bflo(gt.x) * (acc[4 * q + 0] + bflo(yo.x) * bias), v1 = bfhi(gt.x) * (acc[4 * q + 1] + bfhi(yo.x) * bias);
;                         const float v2 = bflo(gt.y) * (acc[4 * q + 2] + bflo(yo.y) * bias), v3 = bfhi(gt.y) * (acc[4 * q + 3] + bfhi(yo.y) * bias);
;                         u32x2 ov; ov.x = pk2(v0, v1); ov.y = pk2(v2, v3);
;                         if (o == 0) *(LAS u32x2*)(Yout + (bb * YSTR + HY_PAD + t0 + 8 * q) * 2) = ov;
;                         else *(u32x2*)(OT + ((size_t)bb * 512 + ch) * KEYS + pos0 + t0 + 8 * q) = ov; } }
.LBB0_771:
	ds_read_b64 v[4:5], v6 offset:48
	v_mov_b32_e32 v6, v28
	v_mov_b32_e32 v7, v30
	v_mov_b32_e32 v30, v29
	s_and_b64 vcc, exec, s[40:41]
	s_waitcnt lgkmcnt(0)
	v_lshlrev_b32_e32 v9, 16, v5
	v_lshlrev_b32_e32 v8, 16, v4
	v_and_b32_e32 v5, 0xffff0000, v5
	v_and_b32_e32 v4, 0xffff0000, v4
	v_pk_fma_f32 v[6:7], v[142:143], v[8:9], v[6:7]
	v_pk_fma_f32 v[4:5], v[142:143], v[4:5], v[30:31]
	s_mov_b64 s[34:35], -1
	v_lshlrev_b32_e32 v9, 16, v205
	v_lshlrev_b32_e32 v8, 16, v204
	v_and_b32_e32 v3, 0xffff0000, v205
	v_and_b32_e32 v2, 0xffff0000, v204
	v_pk_mul_f32 v[2:3], v[4:5], v[2:3]
	v_pk_mul_f32 v[6:7], v[6:7], v[8:9]
	v_and_b32_sdwa v8, v3, v227 dst_sel:DWORD dst_unused:UNUSED_PAD src0_sel:WORD_1 src1_sel:DWORD
	v_and_b32_sdwa v9, v2, v227 dst_sel:DWORD dst_unused:UNUSED_PAD src0_sel:WORD_1 src1_sel:DWORD
	v_and_b32_sdwa v4, v7, v227 dst_sel:DWORD dst_unused:UNUSED_PAD src0_sel:WORD_1 src1_sel:DWORD
	v_and_b32_sdwa v5, v6, v227 dst_sel:DWORD dst_unused:UNUSED_PAD src0_sel:WORD_1 src1_sel:DWORD
	v_add3_u32 v3, v3, v8, s23
	v_add3_u32 v2, v2, v9, s23
	v_add3_u32 v5, v6, v5, s23
	v_add3_u32 v4, v7, v4, s23
	v_and_b32_e32 v3, 0xffff0000, v3
	v_and_b32_e32 v2, 0xffff0000, v2
	v_or_b32_sdwa v3, v3, v4 dst_sel:DWORD dst_unused:UNUSED_PAD src0_sel:DWORD src1_sel:WORD_1
	v_or_b32_sdwa v2, v2, v5 dst_sel:DWORD dst_unused:UNUSED_PAD src0_sel:DWORD src1_sel:WORD_1
	s_cbranch_vccnz .LBB0_773
	s_mov_b64 s[34:35], 0
	global_store_dwordx2 v[140:141], v[2:3], off offset:48

; __device__ __forceinline__ unsigned cvt_pk_bf16(float lo, float hi) { unsigned r; asm volatile("v_cvt_pk_bf16_f32 %0, %1, %2" : "=v"(r) : "v"(lo), "v"(hi)); return r; }
;     __device__ __forceinline__ void operator()(const f32x4 (&acc)[2][2][4][2], const Unit& u, int wr, int wc, int fr, int fq) const {
;         const int row0 = u.pm * BM + wr * 64 + fr, col0 = u.pn * BM + wc * 32 + 8 * fq;
;         const float* ga = mod + (size_t)modrow_of(u.pm * BM) * 12288 + 2 * D;
;         constexpr float sc = WOUT_F8 ? 1.f / 32.f : 1.f;
;         f32x4 gv[2][2];
; #pragma unroll
;         for (int bj = 0; bj < 2; ++bj)
; #pragma unroll
;             for (int n = 0; n < 2; ++n) gv[bj][n] = *(const f32x4*)(ga + col0 + bj * HALF + n * 4) * sc;
;         if (resb) {
; #pragma unroll
;             for (int ai = 0; ai < 2; ++ai)
; #pragma unroll
;                 for (int m = 0; m < 4; ++m) { const int row = row0 + ai * HALF + m * 16; const bf16_t* rp = resb + (size_t)row * D + col0; bf16_t* xp = X + (size_t)row * D + col0;
; #pragma unroll
;                     for (int bj = 0; bj < 2; ++bj) { const u32x4 r = *(const u32x4*)(rp + bj * HALF);
;                         const f32x4 v0 = (f32x4){bflo(r.x), bfhi(r.x), bflo(r.y), bfhi(r.y)} + gv[bj][0] * acc[ai][bj][m][0], v1 = (f32x4){bflo(r.z), bfhi(r.z), bflo(r.w), bfhi(r.w)} + gv[bj][1] * acc[ai][bj][m][1];
;                         u32x4 o; o.x = cvt_pk_bf16(v0[0], v0[1]); o.y = cvt_pk_bf16(v0[2], v0[3]); o.z = cvt_pk_bf16(v1[0], v1[1]); o.w = cvt_pk_bf16(v1[2], v1[3]);
;                         *(u32x4*)(xp + bj * HALF) = o; } }
.LBB0_923:
	s_lshl_b32 s37, s54, 8
	s_min_i32 s34, s37, 0x4000
	s_ashr_i32 s34, s34, 11
	s_mul_hi_i32 s35, s34, 0xc000
	s_mul_i32 s34, s34, 0xc000
	v_lshl_or_b32 v6, s52, 8, v181
	s_add_u32 s34, s74, s34
	s_addc_u32 s35, s75, s35
	v_ashrrev_i32_e32 v7, 31, v6
	v_lshl_add_u64 v[8:9], v[6:7], 2, s[34:35]
	s_mov_b32 s34, 0x104000
	v_add_co_u32_e32 v2, vcc, s34, v8
	s_mov_b64 s[34:35], 0x104000
	s_nop 15
	s_nop 15
	s_nop 0
	v_addc_co_u32_e32 v3, vcc, 0, v9, vcc
	v_lshl_add_u64 v[12:13], v[8:9], 0, s[34:35]
	global_load_dwordx4 v[2:5], v[2:3], off
	s_nop 0
	global_load_dwordx4 v[8:11], v[12:13], off offset:16
	global_load_dwordx4 v[170:173], v[12:13], off offset:512
	global_load_dwordx4 v[174:177], v[12:13], off offset:528
	v_readlane_b32 s56, v254, 32
	v_add_u32_e32 v24, s37, v178
	v_readlane_b32 s57, v254, 33
	s_mov_b64 s[34:35], -1
	v_or_b32_e32 v30, 16, v24
	v_or_b32_e32 v28, 32, v24
	s_andn2_b64 vcc, exec, s[56:57]
	v_or_b32_e32 v26, 48, v24
	s_waitcnt vmcnt(0)
	v_pk_mul_f32 v[16:17], v[10:11], s[20:21] op_sel_hi:[1,0]
	v_pk_mul_f32 v[20:21], v[4:5], s[20:21] op_sel_hi:[1,0]
	v_pk_mul_f32 v[22:23], v[2:3], s[20:21] op_sel_hi:[1,0]
	v_pk_mul_f32 v[18:19], v[8:9], s[20:21] op_sel_hi:[1,0]
	v_pk_mul_f32 v[12:13], v[172:173], s[20:21] op_sel_hi:[1,0]
	v_pk_mul_f32 v[14:15], v[170:171], s[20:21] op_sel_hi:[1,0]
	v_pk_mul_f32 v[8:9], v[176:177], s[20:21] op_sel_hi:[1,0]
	v_pk_mul_f32 v[10:11], v[174:175], s[20:21] op_sel_hi:[1,0]
	s_cbranch_vccnz .LBB0_925
	v_ashrrev_i32_e32 v25, 31, v24
	v_lshlrev_b64 v[186:187], 12, v[24:25]
	v_lshl_add_u64 v[32:33], s[38:39], 0, v[186:187]
	v_lshl_add_u64 v[32:33], v[6:7], 1, v[32:33]
	global_load_dwordx4 v[190:193], v[32:33], off
	global_load_dwordx4 v[196:199], v[32:33], off offset:256
	s_mov_b64 s[34:35], 0x10000
	v_lshl_add_u64 v[184:185], v[32:33], 0, s[34:35]
	global_load_dwordx4 v[200:203], v[184:185], off
	global_load_dwordx4 v[204:207], v[184:185], off offset:256
	s_mov_b64 s[34:35], 0x20000
	v_lshl_add_u64 v[184:185], v[32:33], 0, s[34:35]
	global_load_dwordx4 v[208:211], v[184:185], off
	global_load_dwordx4 v[212:215], v[184:185], off offset:256
	s_mov_b64 s[34:35], 0x30000
	v_lshl_add_u64 v[184:185], v[32:33], 0, s[34:35]
	global_load_dwordx4 v[216:219], v[184:185], off
	global_load_dwordx4 v[220:223], v[184:185], off offset:256
	s_mov_b64 s[34:35], 0x80000
	v_lshl_add_u64 v[184:185], v[32:33], 0, s[34:35]
	global_load_dwordx4 v[242:245], v[184:185], off
	global_load_dwordx4 v[246:249], v[184:185], off offset:256
	s_waitcnt vmcnt(9)
	v_lshlrev_b32_e32 v170, 16, v190
	v_and_b32_e32 v171, 0xffff0000, v190
	v_lshlrev_b32_e32 v172, 16, v191
	v_and_b32_e32 v173, 0xffff0000, v191
	v_lshlrev_b32_e32 v174, 16, v192
	v_and_b32_e32 v175, 0xffff0000, v192
	v_lshlrev_b32_e32 v176, 16, v193
	v_and_b32_e32 v177, 0xffff0000, v193
	v_pk_fma_f32 v[170:171], v[158:159], v[22:23], v[170:171]
	v_pk_fma_f32 v[172:173], v[160:161], v[20:21], v[172:173]
	v_pk_fma_f32 v[174:175], v[154:155], v[18:19], v[174:175]
	v_pk_fma_f32 v[176:177], v[156:157], v[16:17], v[176:177]
	v_cvt_pk_bf16_f32 v170, v170, v171
	v_cvt_pk_bf16_f32 v171, v172, v173
	v_cvt_pk_bf16_f32 v172, v174, v175
	v_cvt_pk_bf16_f32 v173, v176, v177
	global_store_dwordx4 v[32:33], v[170:173], off
	s_nop 1
	s_mov_b64 s[34:35], 0x90000
	v_lshl_add_u64 v[184:185], v[32:33], 0, s[34:35]
	global_load_dwordx4 v[190:193], v[184:185], off
	global_load_dwordx4 v[158:161], v[184:185], off offset:256
	s_mov_b64 s[34:35], 0xa0000
	v_lshl_add_u64 v[184:185], v[32:33], 0, s[34:35]
	global_load_dwordx4 v[154:157], v[184:185], off
	s_waitcnt vmcnt(12)
	v_lshlrev_b32_e32 v170, 16, v196
	v_and_b32_e32 v171, 0xffff0000, v196
	v_lshlrev_b32_e32 v172, 16, v197
	v_and_b32_e32 v173, 0xffff0000, v197
	v_lshlrev_b32_e32 v174, 16, v198
	v_and_b32_e32 v175, 0xffff0000, v198
	v_lshlrev_b32_e32 v176, 16, v199
	v_and_b32_e32 v177, 0xffff0000, v199
	v_pk_fma_f32 v[170:171], v[150:151], v[14:15], v[170:171]
	v_pk_fma_f32 v[172:173], v[152:153], v[12:13], v[172:173]
	v_pk_fma_f32 v[174:175], v[146:147], v[10:11], v[174:175]
	v_pk_fma_f32 v[176:177], v[148:149], v[8:9], v[176:177]
	v_cvt_pk_bf16_f32 v170, v170, v171
	v_cvt_pk_bf16_f32 v171, v172, v173
	v_cvt_pk_bf16_f32 v172, v174, v175
	v_cvt_pk_bf16_f32 v173, v176, v177
	global_store_dwordx4 v[32:33], v[170:173], off offset:256
	s_nop 1
	global_load_dwordx4 v[196:199], v[184:185], off offset:256
	s_mov_b64 s[34:35], 0xb0000
	v_lshl_add_u64 v[184:185], v[32:33], 0, s[34:35]
	global_load_dwordx4 v[150:153], v[184:185], off
	global_load_dwordx4 v[146:149], v[184:185], off offset:256
	s_waitcnt vmcnt(15)
	v_lshlrev_b32_e32 v170, 16, v200
	v_and_b32_e32 v171, 0xffff0000, v200
	v_lshlrev_b32_e32 v172, 16, v201
	v_and_b32_e32 v173, 0xffff0000, v201
	v_lshlrev_b32_e32 v174, 16, v202
	v_and_b32_e32 v175, 0xffff0000, v202
	v_lshlrev_b32_e32 v176, 16, v203
	v_and_b32_e32 v177, 0xffff0000, v203
	v_pk_fma_f32 v[170:171], v[142:143], v[22:23], v[170:171]
	v_pk_fma_f32 v[172:173], v[144:145], v[20:21], v[172:173]
	v_pk_fma_f32 v[174:175], v[138:139], v[18:19], v[174:175]
	v_pk_fma_f32 v[176:177], v[140:141], v[16:17], v[176:177]
	v_cvt_pk_bf16_f32 v170, v170, v171
	v_cvt_pk_bf16_f32 v171, v172, v173
	v_cvt_pk_bf16_f32 v172, v174, v175
	v_cvt_pk_bf16_f32 v173, v176, v177
	s_mov_b64 s[34:35], 0x10000
	v_lshl_add_u64 v[188:189], v[32:33], 0, s[34:35]
	global_store_dwordx4 v[188:189], v[170:173], off
	s_nop 1
	s_waitcnt vmcnt(15)
; __device__ __forceinline__ unsigned cvt_pk_bf16(float lo, float hi) { unsigned r; asm volatile("v_cvt_pk_bf16_f32 %0, %1, %2" : "=v"(r) : "v"(lo), "v"(hi)); return r; }
;     __device__ __forceinline__ void operator()(const f32x4 (&acc)[2][2][4][2], const Unit& u, int wr, int wc, int fr, int fq) const {
;     ...
;                 for (int m = 0; m < 4; ++m) { const int row = row0 + ai * HALF + m * 16; const bf16_t* rp = resb + (size_t)row * D + col0; bf16_t* xp = X + (size_t)row * D + col0;
; #pragma unroll
;                     for (int bj = 0; bj < 2; ++bj) { const u32x4 r = *(const u32x4*)(rp + bj * HALF);
;                         const f32x4 v0 = (f32x4){bflo(r.x), bfhi(r.x), bflo(r.y), bfhi(r.y)} + gv[bj][0] * acc[ai][bj][m][0], v1 = (f32x4){bflo(r.z), bfhi(r.z), bflo(r.w), bfhi(r.w)} + gv[bj][1] * acc[ai][bj][m][1];
;                         u32x4 o; o.x = cvt_pk_bf16(v0[0], v0[1]); o.y = cvt_pk_bf16(v0[2], v0[3]); o.z = cvt_pk_bf16(v1[0], v1[1]); o.w = cvt_pk_bf16(v1[2], v1[3]);
;                         *(u32x4*)(xp + bj * HALF) = o; } }
	v_lshlrev_b32_e32 v170, 16, v204
	v_and_b32_e32 v171, 0xffff0000, v204
	v_lshlrev_b32_e32 v172, 16, v205
	v_and_b32_e32 v173, 0xffff0000, v205
	v_lshlrev_b32_e32 v174, 16, v206
	v_and_b32_e32 v175, 0xffff0000, v206
	v_lshlrev_b32_e32 v176, 16, v207
	v_and_b32_e32 v177, 0xffff0000, v207
	v_pk_fma_f32 v[170:171], v[134:135], v[14:15], v[170:171]
	v_pk_fma_f32 v[172:173], v[136:137], v[12:13], v[172:173]
	v_pk_fma_f32 v[174:175], v[130:131], v[10:11], v[174:175]
	v_pk_fma_f32 v[176:177], v[132:133], v[8:9], v[176:177]
	v_cvt_pk_bf16_f32 v170, v170, v171
	v_cvt_pk_bf16_f32 v171, v172, v173
	v_cvt_pk_bf16_f32 v172, v174, v175
	v_cvt_pk_bf16_f32 v173, v176, v177
	global_store_dwordx4 v[188:189], v[170:173], off offset:256
	s_nop 1
	s_waitcnt vmcnt(15)
	v_lshlrev_b32_e32 v170, 16, v208
	v_and_b32_e32 v171, 0xffff0000, v208
	v_lshlrev_b32_e32 v172, 16, v209
	v_and_b32_e32 v173, 0xffff0000, v209
	v_lshlrev_b32_e32 v174, 16, v210
	v_and_b32_e32 v175, 0xffff0000, v210
	v_lshlrev_b32_e32 v176, 16, v211
	v_and_b32_e32 v177, 0xffff0000, v211
	v_pk_fma_f32 v[170:171], v[126:127], v[22:23], v[170:171]
	v_pk_fma_f32 v[172:173], v[128:129], v[20:21], v[172:173]
	v_pk_fma_f32 v[174:175], v[122:123], v[18:19], v[174:175]
	v_pk_fma_f32 v[176:177], v[124:125], v[16:17], v[176:177]
	v_cvt_pk_bf16_f32 v170, v170, v171
	v_cvt_pk_bf16_f32 v171, v172, v173
	v_cvt_pk_bf16_f32 v172, v174, v175
	v_cvt_pk_bf16_f32 v173, v176, v177
	s_mov_b64 s[34:35], 0x20000
	v_lshl_add_u64 v[188:189], v[32:33], 0, s[34:35]
	global_store_dwordx4 v[188:189], v[170:173], off
	s_nop 1
	s_waitcnt vmcnt(15)
	v_lshlrev_b32_e32 v170, 16, v212
	v_and_b32_e32 v171, 0xffff0000, v212
	v_lshlrev_b32_e32 v172, 16, v213
	v_and_b32_e32 v173, 0xffff0000, v213
	v_lshlrev_b32_e32 v174, 16, v214
	v_and_b32_e32 v175, 0xffff0000, v214
	v_lshlrev_b32_e32 v176, 16, v215
	v_and_b32_e32 v177, 0xffff0000, v215
	v_pk_fma_f32 v[170:171], v[118:119], v[14:15], v[170:171]
	v_pk_fma_f32 v[172:173], v[120:121], v[12:13], v[172:173]
	v_pk_fma_f32 v[174:175], v[114:115], v[10:11], v[174:175]
	v_pk_fma_f32 v[176:177], v[116:117], v[8:9], v[176:177]
	v_cvt_pk_bf16_f32 v170, v170, v171
	v_cvt_pk_bf16_f32 v171, v172, v173
	v_cvt_pk_bf16_f32 v172, v174, v175
	v_cvt_pk_bf16_f32 v173, v176, v177
	global_store_dwordx4 v[188:189], v[170:173], off offset:256
	s_nop 1
	s_waitcnt vmcnt(15)
	v_lshlrev_b32_e32 v170, 16, v216
	v_and_b32_e32 v171, 0xffff0000, v216
	v_lshlrev_b32_e32 v172, 16, v217
	v_and_b32_e32 v173, 0xffff0000, v217
	v_lshlrev_b32_e32 v174, 16, v218
	v_and_b32_e32 v175, 0xffff0000, v218
	v_lshlrev_b32_e32 v176, 16, v219
	v_and_b32_e32 v177, 0xffff0000, v219
	v_pk_fma_f32 v[170:171], v[110:111], v[22:23], v[170:171]
	v_pk_fma_f32 v[172:173], v[112:113], v[20:21], v[172:173]
	v_pk_fma_f32 v[174:175], v[106:107], v[18:19], v[174:175]
	v_pk_fma_f32 v[176:177], v[108:109], v[16:17], v[176:177]
	v_cvt_pk_bf16_f32 v170, v170, v171
	v_cvt_pk_bf16_f32 v171, v172, v173
	v_cvt_pk_bf16_f32 v172, v174, v175
	v_cvt_pk_bf16_f32 v173, v176, v177
	s_mov_b64 s[34:35], 0x30000
	v_lshl_add_u64 v[188:189], v[32:33], 0, s[34:35]
	global_store_dwordx4 v[188:189], v[170:173], off
	s_nop 1
	s_waitcnt vmcnt(15)
	v_lshlrev_b32_e32 v170, 16, v220
	v_and_b32_e32 v171, 0xffff0000, v220
	v_lshlrev_b32_e32 v172, 16, v221
	v_and_b32_e32 v173, 0xffff0000, v221
	v_lshlrev_b32_e32 v174, 16, v222
	v_and_b32_e32 v175, 0xffff0000, v222
	v_lshlrev_b32_e32 v176, 16, v223
	v_and_b32_e32 v177, 0xffff0000, v223
	v_pk_fma_f32 v[170:171], v[102:103], v[14:15], v[170:171]
	v_pk_fma_f32 v[172:173], v[104:105], v[12:13], v[172:173]
	v_pk_fma_f32 v[174:175], v[98:99], v[10:11], v[174:175]
	v_pk_fma_f32 v[176:177], v[100:101], v[8:9], v[176:177]
	v_cvt_pk_bf16_f32 v170, v170, v171
	v_cvt_pk_bf16_f32 v171, v172, v173
	v_cvt_pk_bf16_f32 v172, v174, v175
	v_cvt_pk_bf16_f32 v173, v176, v177
	global_store_dwordx4 v[188:189], v[170:173], off offset:256
	s_nop 1
	s_waitcnt vmcnt(15)
	v_lshlrev_b32_e32 v170, 16, v242
	v_and_b32_e32 v171, 0xffff0000, v242
	v_lshlrev_b32_e32 v172, 16, v243
	v_and_b32_e32 v173, 0xffff0000, v243
	v_lshlrev_b32_e32 v174, 16, v244
	v_and_b32_e32 v175, 0xffff0000, v244
	v_lshlrev_b32_e32 v176, 16, v245
	v_and_b32_e32 v177, 0xffff0000, v245
	v_pk_fma_f32 v[170:171], v[94:95], v[22:23], v[170:171]
	v_pk_fma_f32 v[172:173], v[96:97], v[20:21], v[172:173]
	v_pk_fma_f32 v[174:175], v[90:91], v[18:19], v[174:175]
	v_pk_fma_f32 v[176:177], v[92:93], v[16:17], v[176:177]
	v_cvt_pk_bf16_f32 v170, v170, v171
	v_cvt_pk_bf16_f32 v171, v172, v173
	v_cvt_pk_bf16_f32 v172, v174, v175
	v_cvt_pk_bf16_f32 v173, v176, v177
	s_mov_b64 s[34:35], 0x80000
	v_lshl_add_u64 v[188:189], v[32:33], 0, s[34:35]
	global_store_dwordx4 v[188:189], v[170:173], off
	s_nop 1
	s_waitcnt vmcnt(15)
	v_lshlrev_b32_e32 v170, 16, v246
	v_and_b32_e32 v171, 0xffff0000, v246
	v_lshlrev_b32_e32 v172, 16, v247
	v_and_b32_e32 v173, 0xffff0000, v247
	v_lshlrev_b32_e32 v174, 16, v248
	v_and_b32_e32 v175, 0xffff0000, v248
	v_lshlrev_b32_e32 v176, 16, v249
	v_and_b32_e32 v177, 0xffff0000, v249
	v_pk_fma_f32 v[170:171], v[86:87], v[14:15], v[170:171]
	v_pk_fma_f32 v[172:173], v[88:89], v[12:13], v[172:173]
	v_pk_fma_f32 v[174:175], v[82:83], v[10:11], v[174:175]
	v_pk_fma_f32 v[176:177], v[84:85], v[8:9], v[176:177]
	v_cvt_pk_bf16_f32 v170, v170, v171
	v_cvt_pk_bf16_f32 v171, v172, v173
	v_cvt_pk_bf16_f32 v172, v174, v175
	v_cvt_pk_bf16_f32 v173, v176, v177
	global_store_dwordx4 v[188:189], v[170:173], off offset:256
	s_nop 1
	s_waitcnt vmcnt(14)
; __device__ __forceinline__ unsigned cvt_pk_bf16(float lo, float hi) { unsigned r; asm volatile("v_cvt_pk_bf16_f32 %0, %1, %2" : "=v"(r) : "v"(lo), "v"(hi)); return r; }
;     __device__ __forceinline__ void operator()(const f32x4 (&acc)[2][2][4][2], const Unit& u, int wr, int wc, int fr, int fq) const {
;     ...
;                 for (int m = 0; m < 4; ++m) { const int row = row0 + ai * HALF + m * 16; const bf16_t* rp = resb + (size_t)row * D + col0; bf16_t* xp = X + (size_t)row * D + col0;
; #pragma unroll
;                     for (int bj = 0; bj < 2; ++bj) { const u32x4 r = *(const u32x4*)(rp + bj * HALF);
;                         const f32x4 v0 = (f32x4){bflo(r.x), bfhi(r.x), bflo(r.y), bfhi(r.y)} + gv[bj][0] * acc[ai][bj][m][0], v1 = (f32x4){bflo(r.z), bfhi(r.z), bflo(r.w), bfhi(r.w)} + gv[bj][1] * acc[ai][bj][m][1];
;                         u32x4 o; o.x = cvt_pk_bf16(v0[0], v0[1]); o.y = cvt_pk_bf16(v0[2], v0[3]); o.z = cvt_pk_bf16(v1[0], v1[1]); o.w = cvt_pk_bf16(v1[2], v1[3]);
;                         *(u32x4*)(xp + bj * HALF) = o; } }
	v_lshlrev_b32_e32 v170, 16, v190
	v_and_b32_e32 v171, 0xffff0000, v190
	v_lshlrev_b32_e32 v172, 16, v191
	v_and_b32_e32 v173, 0xffff0000, v191
	v_lshlrev_b32_e32 v174, 16, v192
	v_and_b32_e32 v175, 0xffff0000, v192
	v_lshlrev_b32_e32 v176, 16, v193
	v_and_b32_e32 v177, 0xffff0000, v193
	v_pk_fma_f32 v[170:171], v[78:79], v[22:23], v[170:171]
	v_pk_fma_f32 v[172:173], v[80:81], v[20:21], v[172:173]
	v_pk_fma_f32 v[174:175], v[74:75], v[18:19], v[174:175]
	v_pk_fma_f32 v[176:177], v[76:77], v[16:17], v[176:177]
	v_cvt_pk_bf16_f32 v170, v170, v171
	v_cvt_pk_bf16_f32 v171, v172, v173
	v_cvt_pk_bf16_f32 v172, v174, v175
	v_cvt_pk_bf16_f32 v173, v176, v177
	s_mov_b64 s[34:35], 0x90000
	v_lshl_add_u64 v[188:189], v[32:33], 0, s[34:35]
	global_store_dwordx4 v[188:189], v[170:173], off
	s_nop 1
	s_waitcnt vmcnt(14)
	v_lshlrev_b32_e32 v170, 16, v158
	v_and_b32_e32 v171, 0xffff0000, v158
	v_lshlrev_b32_e32 v172, 16, v159
	v_and_b32_e32 v173, 0xffff0000, v159
	v_lshlrev_b32_e32 v174, 16, v160
	v_and_b32_e32 v175, 0xffff0000, v160
	v_lshlrev_b32_e32 v176, 16, v161
	v_and_b32_e32 v177, 0xffff0000, v161
	v_pk_fma_f32 v[170:171], v[70:71], v[14:15], v[170:171]
	v_pk_fma_f32 v[172:173], v[72:73], v[12:13], v[172:173]
	v_pk_fma_f32 v[174:175], v[66:67], v[10:11], v[174:175]
	v_pk_fma_f32 v[176:177], v[68:69], v[8:9], v[176:177]
	v_cvt_pk_bf16_f32 v170, v170, v171
	v_cvt_pk_bf16_f32 v171, v172, v173
	v_cvt_pk_bf16_f32 v172, v174, v175
	v_cvt_pk_bf16_f32 v173, v176, v177
	global_store_dwordx4 v[188:189], v[170:173], off offset:256
	s_nop 1
	s_waitcnt vmcnt(14)
	v_lshlrev_b32_e32 v170, 16, v154
	v_and_b32_e32 v171, 0xffff0000, v154
	v_lshlrev_b32_e32 v172, 16, v155
	v_and_b32_e32 v173, 0xffff0000, v155
	v_lshlrev_b32_e32 v174, 16, v156
	v_and_b32_e32 v175, 0xffff0000, v156
	v_lshlrev_b32_e32 v176, 16, v157
	v_and_b32_e32 v177, 0xffff0000, v157
	v_pk_fma_f32 v[170:171], v[62:63], v[22:23], v[170:171]
	v_pk_fma_f32 v[172:173], v[64:65], v[20:21], v[172:173]
	v_pk_fma_f32 v[174:175], v[58:59], v[18:19], v[174:175]
	v_pk_fma_f32 v[176:177], v[60:61], v[16:17], v[176:177]
	v_cvt_pk_bf16_f32 v170, v170, v171
	v_cvt_pk_bf16_f32 v171, v172, v173
	v_cvt_pk_bf16_f32 v172, v174, v175
	v_cvt_pk_bf16_f32 v173, v176, v177
	s_mov_b64 s[34:35], 0xa0000
	v_lshl_add_u64 v[188:189], v[32:33], 0, s[34:35]
	global_store_dwordx4 v[188:189], v[170:173], off
	s_nop 1
	s_waitcnt vmcnt(13)
	v_lshlrev_b32_e32 v170, 16, v196
	v_and_b32_e32 v171, 0xffff0000, v196
	v_lshlrev_b32_e32 v172, 16, v197
	v_and_b32_e32 v173, 0xffff0000, v197
	v_lshlrev_b32_e32 v174, 16, v198
	v_and_b32_e32 v175, 0xffff0000, v198
	v_lshlrev_b32_e32 v176, 16, v199
	v_and_b32_e32 v177, 0xffff0000, v199
	v_pk_fma_f32 v[170:171], v[54:55], v[14:15], v[170:171]
	v_pk_fma_f32 v[172:173], v[56:57], v[12:13], v[172:173]
	v_pk_fma_f32 v[174:175], v[50:51], v[10:11], v[174:175]
	v_pk_fma_f32 v[176:177], v[52:53], v[8:9], v[176:177]
	v_cvt_pk_bf16_f32 v170, v170, v171
	v_cvt_pk_bf16_f32 v171, v172, v173
	v_cvt_pk_bf16_f32 v172, v174, v175
	v_cvt_pk_bf16_f32 v173, v176, v177
	global_store_dwordx4 v[188:189], v[170:173], off offset:256
	s_nop 1
	s_waitcnt vmcnt(13)
	v_lshlrev_b32_e32 v170, 16, v150
	v_and_b32_e32 v171, 0xffff0000, v150
	v_lshlrev_b32_e32 v172, 16, v151
	v_and_b32_e32 v173, 0xffff0000, v151
	v_lshlrev_b32_e32 v174, 16, v152
	v_and_b32_e32 v175, 0xffff0000, v152
	v_lshlrev_b32_e32 v176, 16, v153
	v_and_b32_e32 v177, 0xffff0000, v153
	v_pk_fma_f32 v[170:171], v[46:47], v[22:23], v[170:171]
	v_pk_fma_f32 v[172:173], v[48:49], v[20:21], v[172:173]
	v_pk_fma_f32 v[174:175], v[42:43], v[18:19], v[174:175]
	v_pk_fma_f32 v[176:177], v[44:45], v[16:17], v[176:177]
	v_cvt_pk_bf16_f32 v170, v170, v171
	v_cvt_pk_bf16_f32 v171, v172, v173
	v_cvt_pk_bf16_f32 v172, v174, v175
	v_cvt_pk_bf16_f32 v173, v176, v177
	s_mov_b64 s[34:35], 0xb0000
	v_lshl_add_u64 v[188:189], v[32:33], 0, s[34:35]
	global_store_dwordx4 v[188:189], v[170:173], off
	s_nop 1
	s_waitcnt vmcnt(13)
	v_lshlrev_b32_e32 v170, 16, v146
	v_and_b32_e32 v171, 0xffff0000, v146
	v_lshlrev_b32_e32 v172, 16, v147
	v_and_b32_e32 v173, 0xffff0000, v147
	v_lshlrev_b32_e32 v174, 16, v148
	v_and_b32_e32 v175, 0xffff0000, v148
	v_lshlrev_b32_e32 v176, 16, v149
	v_and_b32_e32 v177, 0xffff0000, v149
	v_pk_fma_f32 v[170:171], v[38:39], v[14:15], v[170:171]
	v_pk_fma_f32 v[172:173], v[40:41], v[12:13], v[172:173]
	v_pk_fma_f32 v[174:175], v[34:35], v[10:11], v[174:175]
	v_pk_fma_f32 v[176:177], v[36:37], v[8:9], v[176:177]
	s_mov_b64 s[34:35], 0xb0000
	v_lshl_add_u64 v[32:33], v[186:187], 0, s[34:35]
	v_cvt_pk_bf16_f32 v2, v170, v171
	v_cvt_pk_bf16_f32 v3, v172, v173
	v_cvt_pk_bf16_f32 v4, v174, v175
	v_cvt_pk_bf16_f32 v5, v176, v177
	s_mov_b64 s[34:35], 0
; __device__ __forceinline__ unsigned cvt_pk_bf16(float lo, float hi) { unsigned r; asm volatile("v_cvt_pk_bf16_f32 %0, %1, %2" : "=v"(r) : "v"(lo), "v"(hi)); return r; }
;     __device__ __forceinline__ void operator()(const f32x4 (&acc)[2][2][4][2], const Unit& u, int wr, int wc, int fr, int fq) const {
;     ...
;         if (resb) {
; #pragma unroll
;             for (int ai = 0; ai < 2; ++ai)
; #pragma unroll
;                 for (int m = 0; m < 4; ++m) { const int row = row0 + ai * HALF + m * 16; const bf16_t* rp = resb + (size_t)row * D + col0; bf16_t* xp = X + (size_t)row * D + col0;
; #pragma unroll
;                     for (int bj = 0; bj < 2; ++bj) { const u32x4 r = *(const u32x4*)(rp + bj * HALF);
;                         const f32x4 v0 = (f32x4){bflo(r.x), bfhi(r.x), bflo(r.y), bfhi(r.y)} + gv[bj][0] * acc[ai][bj][m][0], v1 = (f32x4){bflo(r.z), bfhi(r.z), bflo(r.w), bfhi(r.w)} + gv[bj][1] * acc[ai][bj][m][1];
;                         u32x4 o; o.x = cvt_pk_bf16(v0[0], v0[1]); o.y = cvt_pk_bf16(v0[2], v0[3]); o.z = cvt_pk_bf16(v1[0], v1[1]); o.w = cvt_pk_bf16(v1[2], v1[3]);
;                         *(u32x4*)(xp + bj * HALF) = o; } }
;         } else {
; #pragma unroll
;             for (int ai = 0; ai < 2; ++ai)
; #pragma unroll
;                 for (int m = 0; m < 4; ++m) { const int row = row0 + ai * HALF + m * 16;
;                     const float* rp = (row < TL ? res_lat + (size_t)row * D : res_ctx + (size_t)(row - TL) * D) + col0; bf16_t* xp = X + (size_t)row * D + col0;
; #pragma unroll
;                     for (int bj = 0; bj < 2; ++bj) { const f32x4 r0 = *(const f32x4*)(rp + bj * HALF), r1 = *(const f32x4*)(rp + bj * HALF + 4);
;                         const f32x4 v0 = r0 + gv[bj][0] * acc[ai][bj][m][0], v1 = r1 + gv[bj][1] * acc[ai][bj][m][1];
;                         u32x4 o; o.x = cvt_pk_bf16(v0[0], v0[1]); o.y = cvt_pk_bf16(v0[2], v0[3]); o.z = cvt_pk_bf16(v1[0], v1[1]); o.w = cvt_pk_bf16(v1[2], v1[3]);
;                         *(u32x4*)(xp + bj * HALF) = o; } }
.LBB0_925:
	s_andn2_b64 vcc, exec, s[34:35]
	v_readlane_b32 s90, v254, 28
	v_readlane_b32 s89, v254, 30
	v_readlane_b32 s91, v254, 29
	s_cbranch_vccnz .LBB0_959
	v_ashrrev_i32_e32 v25, 31, v24
	v_lshlrev_b64 v[186:187], 12, v[24:25]
	v_lshl_add_u64 v[32:33], s[38:39], 0, v[186:187]
	v_lshl_add_u64 v[32:33], v[6:7], 1, v[32:33]
	v_lshlrev_b64 v[2:3], 13, v[24:25]
	v_lshl_add_u64 v[2:3], s[8:9], 0, v[2:3]
	v_add_u32_e32 v4, 0xffffc000, v24
	v_mov_b32_e32 v5, v0
	v_lshlrev_b64 v[4:5], 13, v[4:5]
	v_lshl_add_u64 v[4:5], s[16:17], 0, v[4:5]
	s_movk_i32 s34, 0x3fff
	v_cmp_lt_i32_e32 vcc, s34, v24
	s_nop 1
	v_cndmask_b32_e32 v2, v2, v4, vcc
	v_cndmask_b32_e32 v3, v3, v5, vcc
	v_lshl_add_u64 v[30:31], v[6:7], 2, v[2:3]
	global_load_dwordx4 v[190:193], v[30:31], off
	global_load_dwordx4 v[196:199], v[30:31], off offset:16
	global_load_dwordx4 v[200:203], v[30:31], off offset:512
	global_load_dwordx4 v[204:207], v[30:31], off offset:528
	s_mov_b64 s[34:35], 0x20000
	v_lshl_add_u64 v[184:185], v[30:31], 0, s[34:35]
	global_load_dwordx4 v[208:211], v[184:185], off
	global_load_dwordx4 v[212:215], v[184:185], off offset:16
	global_load_dwordx4 v[216:219], v[184:185], off offset:512
	global_load_dwordx4 v[220:223], v[184:185], off offset:528
	s_mov_b64 s[34:35], 0x40000
	v_lshl_add_u64 v[184:185], v[30:31], 0, s[34:35]
	global_load_dwordx4 v[242:245], v[184:185], off
	global_load_dwordx4 v[246:249], v[184:185], off offset:16
	s_waitcnt vmcnt(8)
	v_pk_fma_f32 v[170:171], v[158:159], v[22:23], v[190:191]
	v_pk_fma_f32 v[172:173], v[160:161], v[20:21], v[192:193]
	v_pk_fma_f32 v[174:175], v[154:155], v[18:19], v[196:197]
	v_pk_fma_f32 v[176:177], v[156:157], v[16:17], v[198:199]
	v_cvt_pk_bf16_f32 v170, v170, v171
	v_cvt_pk_bf16_f32 v171, v172, v173
	v_cvt_pk_bf16_f32 v172, v174, v175
	v_cvt_pk_bf16_f32 v173, v176, v177
	global_store_dwordx4 v[32:33], v[170:173], off
	s_nop 1
	global_load_dwordx4 v[190:193], v[184:185], off offset:512
	global_load_dwordx4 v[196:199], v[184:185], off offset:528
	s_mov_b64 s[34:35], 0x60000
	v_lshl_add_u64 v[184:185], v[30:31], 0, s[34:35]
	global_load_dwordx4 v[158:161], v[184:185], off
	global_load_dwordx4 v[154:157], v[184:185], off offset:16
	s_waitcnt vmcnt(11)
	v_pk_fma_f32 v[170:171], v[150:151], v[14:15], v[200:201]
	v_pk_fma_f32 v[172:173], v[152:153], v[12:13], v[202:203]
	v_pk_fma_f32 v[174:175], v[146:147], v[10:11], v[204:205]
	v_pk_fma_f32 v[176:177], v[148:149], v[8:9], v[206:207]
	v_cvt_pk_bf16_f32 v170, v170, v171
	v_cvt_pk_bf16_f32 v171, v172, v173
	v_cvt_pk_bf16_f32 v172, v174, v175
	v_cvt_pk_bf16_f32 v173, v176, v177
	global_store_dwordx4 v[32:33], v[170:173], off offset:256
	s_nop 1
	global_load_dwordx4 v[200:203], v[184:185], off offset:512
	global_load_dwordx4 v[204:207], v[184:185], off offset:528
	s_mov_b64 s[34:35], 0x100000
	v_lshl_add_u64 v[184:185], v[30:31], 0, s[34:35]
	global_load_dwordx4 v[150:153], v[184:185], off
	global_load_dwordx4 v[146:149], v[184:185], off offset:16
	s_waitcnt vmcnt(14)
	v_pk_fma_f32 v[170:171], v[142:143], v[22:23], v[208:209]
	v_pk_fma_f32 v[172:173], v[144:145], v[20:21], v[210:211]
	v_pk_fma_f32 v[174:175], v[138:139], v[18:19], v[212:213]
	v_pk_fma_f32 v[176:177], v[140:141], v[16:17], v[214:215]
	v_cvt_pk_bf16_f32 v170, v170, v171
	v_cvt_pk_bf16_f32 v171, v172, v173
	v_cvt_pk_bf16_f32 v172, v174, v175
	v_cvt_pk_bf16_f32 v173, v176, v177
	s_mov_b64 s[34:35], 0x10000
	v_lshl_add_u64 v[188:189], v[32:33], 0, s[34:35]
	global_store_dwordx4 v[188:189], v[170:173], off
	s_nop 1
	global_load_dwordx4 v[208:211], v[184:185], off offset:512
	global_load_dwordx4 v[212:215], v[184:185], off offset:528
	s_mov_b64 s[34:35], 0x120000
	v_lshl_add_u64 v[184:185], v[30:31], 0, s[34:35]
	global_load_dwordx4 v[142:145], v[184:185], off
	global_load_dwordx4 v[138:141], v[184:185], off offset:16
	s_waitcnt vmcnt(17)
	v_pk_fma_f32 v[170:171], v[134:135], v[14:15], v[216:217]
	v_pk_fma_f32 v[172:173], v[136:137], v[12:13], v[218:219]
	v_pk_fma_f32 v[174:175], v[130:131], v[10:11], v[220:221]
	v_pk_fma_f32 v[176:177], v[132:133], v[8:9], v[222:223]
	v_cvt_pk_bf16_f32 v170, v170, v171
	v_cvt_pk_bf16_f32 v171, v172, v173
	v_cvt_pk_bf16_f32 v172, v174, v175
	v_cvt_pk_bf16_f32 v173, v176, v177
	global_store_dwordx4 v[188:189], v[170:173], off offset:256
	s_nop 1
	global_load_dwordx4 v[216:219], v[184:185], off offset:512
	global_load_dwordx4 v[220:223], v[184:185], off offset:528
	s_mov_b64 s[34:35], 0x140000
	v_lshl_add_u64 v[184:185], v[30:31], 0, s[34:35]
	global_load_dwordx4 v[134:137], v[184:185], off
	global_load_dwordx4 v[130:133], v[184:185], off offset:16
	s_waitcnt vmcnt(20)
	v_pk_fma_f32 v[170:171], v[126:127], v[22:23], v[242:243]
	v_pk_fma_f32 v[172:173], v[128:129], v[20:21], v[244:245]
	v_pk_fma_f32 v[174:175], v[122:123], v[18:19], v[246:247]
	v_pk_fma_f32 v[176:177], v[124:125], v[16:17], v[248:249]
	v_cvt_pk_bf16_f32 v170, v170, v171
	v_cvt_pk_bf16_f32 v171, v172, v173
	v_cvt_pk_bf16_f32 v172, v174, v175
	v_cvt_pk_bf16_f32 v173, v176, v177
	s_mov_b64 s[34:35], 0x20000
	v_lshl_add_u64 v[188:189], v[32:33], 0, s[34:35]
	global_store_dwordx4 v[188:189], v[170:173], off
	s_nop 1
	global_load_dwordx4 v[242:245], v[184:185], off offset:512
	global_load_dwordx4 v[246:249], v[184:185], off offset:528
	s_mov_b64 s[34:35], 0x160000
	v_lshl_add_u64 v[184:185], v[30:31], 0, s[34:35]
	global_load_dwordx4 v[126:129], v[184:185], off
	global_load_dwordx4 v[122:125], v[184:185], off offset:16
	s_waitcnt vmcnt(22)
; __device__ __forceinline__ unsigned cvt_pk_bf16(float lo, float hi) { unsigned r; asm volatile("v_cvt_pk_bf16_f32 %0, %1, %2" : "=v"(r) : "v"(lo), "v"(hi)); return r; }
;     __device__ __forceinline__ void operator()(const f32x4 (&acc)[2][2][4][2], const Unit& u, int wr, int wc, int fr, int fq) const {
;     ...
;             for (int ai = 0; ai < 2; ++ai)
; #pragma unroll
;                 for (int m = 0; m < 4; ++m) { const int row = row0 + ai * HALF + m * 16;
;                     const float* rp = (row < TL ? res_lat + (size_t)row * D : res_ctx + (size_t)(row - TL) * D) + col0; bf16_t* xp = X + (size_t)row * D + col0;
; #pragma unroll
;                     for (int bj = 0; bj < 2; ++bj) { const f32x4 r0 = *(const f32x4*)(rp + bj * HALF), r1 = *(const f32x4*)(rp + bj * HALF + 4);
;                         const f32x4 v0 = r0 + gv[bj][0] * acc[ai][bj][m][0], v1 = r1 + gv[bj][1] * acc[ai][bj][m][1];
;                         u32x4 o; o.x = cvt_pk_bf16(v0[0], v0[1]); o.y = cvt_pk_bf16(v0[2], v0[3]); o.z = cvt_pk_bf16(v1[0], v1[1]); o.w = cvt_pk_bf16(v1[2], v1[3]);
;                         *(u32x4*)(xp + bj * HALF) = o; } }
	v_pk_fma_f32 v[170:171], v[118:119], v[14:15], v[190:191]
	v_pk_fma_f32 v[172:173], v[120:121], v[12:13], v[192:193]
	v_pk_fma_f32 v[174:175], v[114:115], v[10:11], v[196:197]
	v_pk_fma_f32 v[176:177], v[116:117], v[8:9], v[198:199]
	v_cvt_pk_bf16_f32 v170, v170, v171
	v_cvt_pk_bf16_f32 v171, v172, v173
	v_cvt_pk_bf16_f32 v172, v174, v175
	v_cvt_pk_bf16_f32 v173, v176, v177
	global_store_dwordx4 v[188:189], v[170:173], off offset:256
	s_nop 1
	global_load_dwordx4 v[190:193], v[184:185], off offset:512
	global_load_dwordx4 v[196:199], v[184:185], off offset:528
	s_waitcnt vmcnt(23)
	v_pk_fma_f32 v[170:171], v[110:111], v[22:23], v[158:159]
	v_pk_fma_f32 v[172:173], v[112:113], v[20:21], v[160:161]
	v_pk_fma_f32 v[174:175], v[106:107], v[18:19], v[154:155]
	v_pk_fma_f32 v[176:177], v[108:109], v[16:17], v[156:157]
	v_cvt_pk_bf16_f32 v170, v170, v171
	v_cvt_pk_bf16_f32 v171, v172, v173
	v_cvt_pk_bf16_f32 v172, v174, v175
	v_cvt_pk_bf16_f32 v173, v176, v177
	s_mov_b64 s[34:35], 0x30000
	v_lshl_add_u64 v[188:189], v[32:33], 0, s[34:35]
	global_store_dwordx4 v[188:189], v[170:173], off
	s_nop 1
	s_waitcnt vmcnt(21)
	v_pk_fma_f32 v[170:171], v[102:103], v[14:15], v[200:201]
	v_pk_fma_f32 v[172:173], v[104:105], v[12:13], v[202:203]
	v_pk_fma_f32 v[174:175], v[98:99], v[10:11], v[204:205]
	v_pk_fma_f32 v[176:177], v[100:101], v[8:9], v[206:207]
	v_cvt_pk_bf16_f32 v170, v170, v171
	v_cvt_pk_bf16_f32 v171, v172, v173
	v_cvt_pk_bf16_f32 v172, v174, v175
	v_cvt_pk_bf16_f32 v173, v176, v177
	global_store_dwordx4 v[188:189], v[170:173], off offset:256
	s_nop 1
	s_waitcnt vmcnt(20)
	v_pk_fma_f32 v[170:171], v[94:95], v[22:23], v[150:151]
	v_pk_fma_f32 v[172:173], v[96:97], v[20:21], v[152:153]
	v_pk_fma_f32 v[174:175], v[90:91], v[18:19], v[146:147]
	v_pk_fma_f32 v[176:177], v[92:93], v[16:17], v[148:149]
	v_cvt_pk_bf16_f32 v170, v170, v171
	v_cvt_pk_bf16_f32 v171, v172, v173
	v_cvt_pk_bf16_f32 v172, v174, v175
	v_cvt_pk_bf16_f32 v173, v176, v177
	s_mov_b64 s[34:35], 0x80000
	v_lshl_add_u64 v[188:189], v[32:33], 0, s[34:35]
	global_store_dwordx4 v[188:189], v[170:173], off
	s_nop 1
	s_waitcnt vmcnt(18)
	v_pk_fma_f32 v[170:171], v[86:87], v[14:15], v[208:209]
	v_pk_fma_f32 v[172:173], v[88:89], v[12:13], v[210:211]
	v_pk_fma_f32 v[174:175], v[82:83], v[10:11], v[212:213]
	v_pk_fma_f32 v[176:177], v[84:85], v[8:9], v[214:215]
	v_cvt_pk_bf16_f32 v170, v170, v171
	v_cvt_pk_bf16_f32 v171, v172, v173
	v_cvt_pk_bf16_f32 v172, v174, v175
	v_cvt_pk_bf16_f32 v173, v176, v177
	global_store_dwordx4 v[188:189], v[170:173], off offset:256
	s_nop 1
	s_waitcnt vmcnt(17)
	v_pk_fma_f32 v[170:171], v[78:79], v[22:23], v[142:143]
	v_pk_fma_f32 v[172:173], v[80:81], v[20:21], v[144:145]
	v_pk_fma_f32 v[174:175], v[74:75], v[18:19], v[138:139]
	v_pk_fma_f32 v[176:177], v[76:77], v[16:17], v[140:141]
	v_cvt_pk_bf16_f32 v170, v170, v171
	v_cvt_pk_bf16_f32 v171, v172, v173
	v_cvt_pk_bf16_f32 v172, v174, v175
	v_cvt_pk_bf16_f32 v173, v176, v177
	s_mov_b64 s[34:35], 0x90000
	v_lshl_add_u64 v[188:189], v[32:33], 0, s[34:35]
	global_store_dwordx4 v[188:189], v[170:173], off
	s_nop 1
	s_waitcnt vmcnt(15)
	v_pk_fma_f32 v[170:171], v[70:71], v[14:15], v[216:217]
	v_pk_fma_f32 v[172:173], v[72:73], v[12:13], v[218:219]
	v_pk_fma_f32 v[174:175], v[66:67], v[10:11], v[220:221]
	v_pk_fma_f32 v[176:177], v[68:69], v[8:9], v[222:223]
	v_cvt_pk_bf16_f32 v170, v170, v171
	v_cvt_pk_bf16_f32 v171, v172, v173
	v_cvt_pk_bf16_f32 v172, v174, v175
	v_cvt_pk_bf16_f32 v173, v176, v177
	global_store_dwordx4 v[188:189], v[170:173], off offset:256
	s_nop 1
	s_waitcnt vmcnt(14)
	v_pk_fma_f32 v[170:171], v[62:63], v[22:23], v[134:135]
	v_pk_fma_f32 v[172:173], v[64:65], v[20:21], v[136:137]
	v_pk_fma_f32 v[174:175], v[58:59], v[18:19], v[130:131]
	v_pk_fma_f32 v[176:177], v[60:61], v[16:17], v[132:133]
	v_cvt_pk_bf16_f32 v170, v170, v171
	v_cvt_pk_bf16_f32 v171, v172, v173
	v_cvt_pk_bf16_f32 v172, v174, v175
	v_cvt_pk_bf16_f32 v173, v176, v177
	s_mov_b64 s[34:35], 0xa0000
	v_lshl_add_u64 v[188:189], v[32:33], 0, s[34:35]
	global_store_dwordx4 v[188:189], v[170:173], off
	s_nop 1
	s_waitcnt vmcnt(12)
	v_pk_fma_f32 v[170:171], v[54:55], v[14:15], v[242:243]
	v_pk_fma_f32 v[172:173], v[56:57], v[12:13], v[244:245]
	v_pk_fma_f32 v[174:175], v[50:51], v[10:11], v[246:247]
	v_pk_fma_f32 v[176:177], v[52:53], v[8:9], v[248:249]
	v_cvt_pk_bf16_f32 v170, v170, v171
	v_cvt_pk_bf16_f32 v171, v172, v173
	v_cvt_pk_bf16_f32 v172, v174, v175
	v_cvt_pk_bf16_f32 v173, v176, v177
	global_store_dwordx4 v[188:189], v[170:173], off offset:256
	s_nop 1
	s_waitcnt vmcnt(11)
	v_pk_fma_f32 v[170:171], v[46:47], v[22:23], v[126:127]
	v_pk_fma_f32 v[172:173], v[48:49], v[20:21], v[128:129]
	v_pk_fma_f32 v[174:175], v[42:43], v[18:19], v[122:123]
	v_pk_fma_f32 v[176:177], v[44:45], v[16:17], v[124:125]
	v_cvt_pk_bf16_f32 v170, v170, v171
	v_cvt_pk_bf16_f32 v171, v172, v173
	v_cvt_pk_bf16_f32 v172, v174, v175
	v_cvt_pk_bf16_f32 v173, v176, v177
	s_mov_b64 s[34:35], 0xb0000
	v_lshl_add_u64 v[188:189], v[32:33], 0, s[34:35]
	global_store_dwordx4 v[188:189], v[170:173], off
	s_nop 1
	s_waitcnt vmcnt(9)
	v_pk_fma_f32 v[170:171], v[38:39], v[14:15], v[190:191]
	v_pk_fma_f32 v[172:173], v[40:41], v[12:13], v[192:193]
	v_pk_fma_f32 v[174:175], v[34:35], v[10:11], v[196:197]
	v_pk_fma_f32 v[176:177], v[36:37], v[8:9], v[198:199]
	s_mov_b64 s[34:35], 0xb0000
	v_lshl_add_u64 v[32:33], v[186:187], 0, s[34:35]
	v_cvt_pk_bf16_f32 v2, v170, v171
	v_cvt_pk_bf16_f32 v3, v172, v173
	v_cvt_pk_bf16_f32 v4, v174, v175
	v_cvt_pk_bf16_f32 v5, v176, v177

;     __device__ __forceinline__ void operator()(const f32x4 (&acc)[2][2][4][2], const Unit& u, int wr, int wc, int fr, int fq) const {
;         const int row0 = u.pm * BM + wr * 64 + fr, col0 = (u.pn & 7) * BM + wc * 32 + 8 * fq;
; #pragma unroll
;         for (int ai = 0; ai < 2; ++ai)
; #pragma unroll
;             for (int m = 0; m < 4; ++m) { asm volatile("" ::: "memory"); const int row = row0 + ai * HALF + m * 16; const int tk = rowtok[row]; const float w = roww[row];
;                 if (tk >= 0) { unsigned char* rowp = Y2 + ((size_t)(tk >> 30) * TT + (size_t)(tk & 0x3fffffff)) * D + col0;
; #pragma unroll
;                     for (int bj = 0; bj < 2; ++bj) { const f32x4 v0 = acc[ai][bj][m][0] * w, v1 = acc[ai][bj][m][1] * w;
;                         u32x2 o; o.x = pk4_f8(v0[0], v0[1], v0[2], v0[3]); o.y = pk4_f8(v1[0], v1[1], v1[2], v1[3]);
;                         *(u32x2*)(rowp + bj * HALF) = o; } } }
;     }
.LBB0_1373:
	v_lshl_add_u32 v8, s37, 8, v178
	s_nop 15
	s_nop 15
	v_ashrrev_i32_e32 v9, 31, v8
	v_lshl_add_u64 v[6:7], v[8:9], 2, s[26:27]
	v_lshl_add_u64 v[4:5], v[8:9], 2, s[38:39]
	global_load_dword v220, v[6:7], off
	global_load_dword v221, v[6:7], off offset:64
	global_load_dword v222, v[6:7], off offset:128
	global_load_dword v223, v[6:7], off offset:192
	global_load_dword v224, v[6:7], off offset:512
	global_load_dword v225, v[6:7], off offset:576
	global_load_dword v228, v[6:7], off offset:640
	global_load_dword v229, v[6:7], off offset:704
	global_load_dword v242, v[4:5], off
	global_load_dword v243, v[4:5], off offset:64
	global_load_dword v244, v[4:5], off offset:128
	global_load_dword v245, v[4:5], off offset:192
	global_load_dword v246, v[4:5], off offset:512
	global_load_dword v247, v[4:5], off offset:576
	global_load_dword v248, v[4:5], off offset:640
	global_load_dword v249, v[4:5], off offset:704
	s_waitcnt vmcnt(0)
	v_mov_b32_e32 v10, v220
	s_lshl_b32 s34, s52, 8
	s_and_b32 s34, s34, 0x700
	v_mov_b32_e32 v3, v0
	v_or_b32_e32 v2, s34, v181
	v_cmp_lt_i32_e32 vcc, -1, v10
	s_and_saveexec_b64 s[34:35], vcc
	s_cbranch_execz .LBB0_1375
	v_mov_b32_e32 v12, v242
	v_lshrrev_b32_e32 v9, 30, v10
	v_and_b32_e32 v10, 0x3fffffff, v10
	s_movk_i32 s37, 0x4800
	v_mad_u32_u24 v10, v9, s37, v10
	v_mov_b32_e32 v11, v0
	v_lshlrev_b64 v[10:11], 11, v[10:11]
	v_lshl_add_u64 v[10:11], s[16:17], 0, v[10:11]
	v_lshl_add_u64 v[10:11], v[10:11], 0, v[2:3]
	v_pk_mul_f32 v[14:15], v[160:161], v[12:13] op_sel_hi:[1,0]
	v_pk_mul_f32 v[16:17], v[158:159], v[12:13] op_sel_hi:[1,0]
	v_pk_mul_f32 v[18:19], v[156:157], v[12:13] op_sel_hi:[1,0]
	v_pk_mul_f32 v[20:21], v[154:155], v[12:13] op_sel_hi:[1,0]
	v_med3_f32 v9, v16, s83, v238
	v_med3_f32 v13, v17, s83, v238
	v_med3_f32 v16, v14, s83, v238
	v_mov_b32_e32 v14, v0
	v_cvt_pk_fp8_f32 v14, v9, v13
	v_med3_f32 v15, v15, s83, v238
	v_med3_f32 v9, v20, s83, v238
	v_med3_f32 v13, v21, s83, v238
	v_cvt_pk_fp8_f32 v14, v16, v15 op_sel:[0,0,1]
	v_mov_b32_e32 v15, v0
	v_cvt_pk_fp8_f32 v15, v9, v13
	v_med3_f32 v16, v18, s83, v238
	v_med3_f32 v17, v19, s83, v238
	v_pk_mul_f32 v[18:19], v[148:149], v[12:13] op_sel_hi:[1,0]
	v_cvt_pk_fp8_f32 v15, v16, v17 op_sel:[0,0,1]
	v_pk_mul_f32 v[16:17], v[150:151], v[12:13] op_sel_hi:[1,0]
	global_store_dwordx2 v[10:11], v[14:15], off
	v_pk_mul_f32 v[14:15], v[152:153], v[12:13] op_sel_hi:[1,0]
	v_med3_f32 v9, v16, s83, v238
	v_med3_f32 v16, v17, s83, v238
	v_med3_f32 v17, v14, s83, v238
	v_mov_b32_e32 v14, v0
	v_cvt_pk_fp8_f32 v14, v9, v16
	v_pk_mul_f32 v[12:13], v[146:147], v[12:13] op_sel_hi:[1,0]
	v_med3_f32 v15, v15, s83, v238
	v_med3_f32 v9, v12, s83, v238
	v_cvt_pk_fp8_f32 v14, v17, v15 op_sel:[0,0,1]
	v_med3_f32 v12, v13, s83, v238
	v_mov_b32_e32 v15, v0
	v_cvt_pk_fp8_f32 v15, v9, v12
	v_med3_f32 v13, v18, s83, v238
	v_med3_f32 v16, v19, s83, v238
	v_cvt_pk_fp8_f32 v15, v13, v16 op_sel:[0,0,1]
	global_store_dwordx2 v[10:11], v[14:15], off offset:128
.LBB0_1375:
	s_or_b64 exec, exec, s[34:35]
	v_or_b32_e32 v10, 16, v8
	v_ashrrev_i32_e32 v11, 31, v10
	v_lshl_add_u64 v[12:13], v[10:11], 2, s[26:27]
	v_mov_b32_e32 v9, v221
	v_cmp_lt_i32_e32 vcc, -1, v9
	s_and_saveexec_b64 s[34:35], vcc
	s_cbranch_execz .LBB0_1377
	v_lshl_add_u64 v[10:11], v[10:11], 2, s[38:39]
	v_mov_b32_e32 v12, v243
	v_lshrrev_b32_e32 v10, 30, v9
	v_and_b32_e32 v9, 0x3fffffff, v9
	s_movk_i32 s37, 0x4800
	v_mad_u32_u24 v10, v10, s37, v9
	v_mov_b32_e32 v11, v0
	v_lshlrev_b64 v[10:11], 11, v[10:11]
	v_lshl_add_u64 v[10:11], s[16:17], 0, v[10:11]
	v_lshl_add_u64 v[10:11], v[10:11], 0, v[2:3]
	v_pk_mul_f32 v[14:15], v[144:145], v[12:13] op_sel_hi:[1,0]
	v_pk_mul_f32 v[16:17], v[142:143], v[12:13] op_sel_hi:[1,0]
	v_pk_mul_f32 v[18:19], v[140:141], v[12:13] op_sel_hi:[1,0]
	v_pk_mul_f32 v[20:21], v[138:139], v[12:13] op_sel_hi:[1,0]
	v_med3_f32 v9, v16, s83, v238
	v_med3_f32 v13, v17, s83, v238
	v_med3_f32 v16, v14, s83, v238
	v_mov_b32_e32 v14, v0
	v_cvt_pk_fp8_f32 v14, v9, v13
	v_med3_f32 v15, v15, s83, v238
	v_med3_f32 v9, v20, s83, v238
	v_med3_f32 v13, v21, s83, v238
	v_cvt_pk_fp8_f32 v14, v16, v15 op_sel:[0,0,1]
	v_mov_b32_e32 v15, v0
	v_cvt_pk_fp8_f32 v15, v9, v13
	v_med3_f32 v16, v18, s83, v238
	v_med3_f32 v17, v19, s83, v238
	v_pk_mul_f32 v[18:19], v[132:133], v[12:13] op_sel_hi:[1,0]
	v_cvt_pk_fp8_f32 v15, v16, v17 op_sel:[0,0,1]
	v_pk_mul_f32 v[16:17], v[134:135], v[12:13] op_sel_hi:[1,0]
	global_store_dwordx2 v[10:11], v[14:15], off
	v_pk_mul_f32 v[14:15], v[136:137], v[12:13] op_sel_hi:[1,0]
	v_med3_f32 v9, v16, s83, v238
	v_med3_f32 v16, v17, s83, v238
	v_med3_f32 v17, v14, s83, v238
	v_mov_b32_e32 v14, v0
	v_cvt_pk_fp8_f32 v14, v9, v16
	v_pk_mul_f32 v[12:13], v[130:131], v[12:13] op_sel_hi:[1,0]
	v_med3_f32 v15, v15, s83, v238
	v_med3_f32 v9, v12, s83, v238
	v_cvt_pk_fp8_f32 v14, v17, v15 op_sel:[0,0,1]
	v_med3_f32 v12, v13, s83, v238
	v_mov_b32_e32 v15, v0
	v_cvt_pk_fp8_f32 v15, v9, v12
	v_med3_f32 v13, v18, s83, v238
	v_med3_f32 v16, v19, s83, v238
	v_cvt_pk_fp8_f32 v15, v13, v16 op_sel:[0,0,1]
	global_store_dwordx2 v[10:11], v[14:15], off offset:128
;     __device__ __forceinline__ void operator()(const f32x4 (&acc)[2][2][4][2], const Unit& u, int wr, int wc, int fr, int fq) const {
;         const int row0 = u.pm * BM + wr * 64 + fr, col0 = (u.pn & 7) * BM + wc * 32 + 8 * fq;
; #pragma unroll
;         for (int ai = 0; ai < 2; ++ai)
; #pragma unroll
;             for (int m = 0; m < 4; ++m) { asm volatile("" ::: "memory"); const int row = row0 + ai * HALF + m * 16; const int tk = rowtok[row]; const float w = roww[row];
;                 if (tk >= 0) { unsigned char* rowp = Y2 + ((size_t)(tk >> 30) * TT + (size_t)(tk & 0x3fffffff)) * D + col0;
; #pragma unroll
;                     for (int bj = 0; bj < 2; ++bj) { const f32x4 v0 = acc[ai][bj][m][0] * w, v1 = acc[ai][bj][m][1] * w;
;                         u32x2 o; o.x = pk4_f8(v0[0], v0[1], v0[2], v0[3]); o.y = pk4_f8(v1[0], v1[1], v1[2], v1[3]);
;                         *(u32x2*)(rowp + bj * HALF) = o; } } }
;     }
.LBB0_1377:
	s_or_b64 exec, exec, s[34:35]
	v_or_b32_e32 v10, 32, v8
	v_ashrrev_i32_e32 v11, 31, v10
	v_lshl_add_u64 v[12:13], v[10:11], 2, s[26:27]
	v_mov_b32_e32 v9, v222
	v_cmp_lt_i32_e32 vcc, -1, v9
	s_and_saveexec_b64 s[34:35], vcc
	s_movk_i32 s75, 0x77
	s_cbranch_execz .LBB0_1379
	v_lshl_add_u64 v[10:11], v[10:11], 2, s[38:39]
	v_mov_b32_e32 v12, v244
	v_lshrrev_b32_e32 v10, 30, v9
	v_and_b32_e32 v9, 0x3fffffff, v9
	s_movk_i32 s37, 0x4800
	v_mad_u32_u24 v10, v10, s37, v9
	v_mov_b32_e32 v11, v0
	v_lshlrev_b64 v[10:11], 11, v[10:11]
	v_lshl_add_u64 v[10:11], s[16:17], 0, v[10:11]
	v_lshl_add_u64 v[10:11], v[10:11], 0, v[2:3]
	v_pk_mul_f32 v[14:15], v[128:129], v[12:13] op_sel_hi:[1,0]
	v_pk_mul_f32 v[16:17], v[126:127], v[12:13] op_sel_hi:[1,0]
	v_pk_mul_f32 v[18:19], v[124:125], v[12:13] op_sel_hi:[1,0]
	v_pk_mul_f32 v[20:21], v[122:123], v[12:13] op_sel_hi:[1,0]
	v_med3_f32 v9, v16, s83, v238
	v_med3_f32 v13, v17, s83, v238
	v_med3_f32 v16, v14, s83, v238
	v_mov_b32_e32 v14, v0
	v_cvt_pk_fp8_f32 v14, v9, v13
	v_med3_f32 v15, v15, s83, v238
	v_med3_f32 v9, v20, s83, v238
	v_med3_f32 v13, v21, s83, v238
	v_cvt_pk_fp8_f32 v14, v16, v15 op_sel:[0,0,1]
	v_mov_b32_e32 v15, v0
	v_cvt_pk_fp8_f32 v15, v9, v13
	v_med3_f32 v16, v18, s83, v238
	v_med3_f32 v17, v19, s83, v238
	v_pk_mul_f32 v[18:19], v[116:117], v[12:13] op_sel_hi:[1,0]
	v_cvt_pk_fp8_f32 v15, v16, v17 op_sel:[0,0,1]
	v_pk_mul_f32 v[16:17], v[118:119], v[12:13] op_sel_hi:[1,0]
	global_store_dwordx2 v[10:11], v[14:15], off
	v_pk_mul_f32 v[14:15], v[120:121], v[12:13] op_sel_hi:[1,0]
	v_med3_f32 v9, v16, s83, v238
	v_med3_f32 v16, v17, s83, v238
	v_med3_f32 v17, v14, s83, v238
	v_mov_b32_e32 v14, v0
	v_cvt_pk_fp8_f32 v14, v9, v16
	v_pk_mul_f32 v[12:13], v[114:115], v[12:13] op_sel_hi:[1,0]
	v_med3_f32 v15, v15, s83, v238
	v_med3_f32 v9, v12, s83, v238
	v_cvt_pk_fp8_f32 v14, v17, v15 op_sel:[0,0,1]
	v_med3_f32 v12, v13, s83, v238
	v_mov_b32_e32 v15, v0
	v_cvt_pk_fp8_f32 v15, v9, v12
	v_med3_f32 v13, v18, s83, v238
	v_med3_f32 v16, v19, s83, v238
	v_cvt_pk_fp8_f32 v15, v13, v16 op_sel:[0,0,1]
	global_store_dwordx2 v[10:11], v[14:15], off offset:128
.LBB0_1379:
	s_or_b64 exec, exec, s[34:35]
	v_or_b32_e32 v8, 48, v8
	v_ashrrev_i32_e32 v9, 31, v8
	v_lshl_add_u64 v[10:11], v[8:9], 2, s[26:27]
	v_mov_b32_e32 v10, v223
	v_cmp_lt_i32_e32 vcc, -1, v10
	s_and_saveexec_b64 s[34:35], vcc
	s_cbranch_execz .LBB0_1381
	v_lshl_add_u64 v[8:9], v[8:9], 2, s[38:39]
	v_mov_b32_e32 v12, v245
	v_lshrrev_b32_e32 v8, 30, v10
	v_and_b32_e32 v9, 0x3fffffff, v10
	s_movk_i32 s37, 0x4800
	v_mad_u32_u24 v8, v8, s37, v9
	v_mov_b32_e32 v9, v0
	v_lshlrev_b64 v[8:9], 11, v[8:9]
	v_lshl_add_u64 v[8:9], s[16:17], 0, v[8:9]
	v_lshl_add_u64 v[8:9], v[8:9], 0, v[2:3]
	v_pk_mul_f32 v[10:11], v[112:113], v[12:13] op_sel_hi:[1,0]
	v_pk_mul_f32 v[14:15], v[110:111], v[12:13] op_sel_hi:[1,0]
	v_pk_mul_f32 v[16:17], v[108:109], v[12:13] op_sel_hi:[1,0]
	v_pk_mul_f32 v[18:19], v[106:107], v[12:13] op_sel_hi:[1,0]
	v_med3_f32 v13, v14, s83, v238
	v_med3_f32 v14, v15, s83, v238
	v_med3_f32 v15, v10, s83, v238
	v_mov_b32_e32 v10, v0
	v_cvt_pk_fp8_f32 v10, v13, v14
	v_med3_f32 v11, v11, s83, v238
	v_med3_f32 v13, v18, s83, v238
	v_med3_f32 v14, v19, s83, v238
	v_cvt_pk_fp8_f32 v10, v15, v11 op_sel:[0,0,1]
	v_mov_b32_e32 v11, v0
	v_cvt_pk_fp8_f32 v11, v13, v14
	v_med3_f32 v15, v16, s83, v238
	v_med3_f32 v16, v17, s83, v238
	v_cvt_pk_fp8_f32 v11, v15, v16 op_sel:[0,0,1]
	v_pk_mul_f32 v[14:15], v[102:103], v[12:13] op_sel_hi:[1,0]
	v_pk_mul_f32 v[16:17], v[100:101], v[12:13] op_sel_hi:[1,0]
	v_med3_f32 v14, v14, s83, v238
	global_store_dwordx2 v[8:9], v[10:11], off
	v_pk_mul_f32 v[10:11], v[104:105], v[12:13] op_sel_hi:[1,0]
	v_med3_f32 v15, v15, s83, v238
	v_med3_f32 v18, v10, s83, v238
	v_mov_b32_e32 v10, v0
	v_cvt_pk_fp8_f32 v10, v14, v15
	v_pk_mul_f32 v[12:13], v[98:99], v[12:13] op_sel_hi:[1,0]
	v_med3_f32 v11, v11, s83, v238
	v_med3_f32 v12, v12, s83, v238
	v_cvt_pk_fp8_f32 v10, v18, v11 op_sel:[0,0,1]
	v_med3_f32 v13, v13, s83, v238
	v_mov_b32_e32 v11, v0
	v_cvt_pk_fp8_f32 v11, v12, v13
	v_med3_f32 v14, v16, s83, v238
	v_med3_f32 v15, v17, s83, v238
	v_cvt_pk_fp8_f32 v11, v14, v15 op_sel:[0,0,1]
	global_store_dwordx2 v[8:9], v[10:11], off offset:128
.LBB0_1381:
	s_or_b64 exec, exec, s[34:35]
	v_mov_b32_e32 v8, v224
	v_cmp_lt_i32_e32 vcc, -1, v8
	s_and_saveexec_b64 s[34:35], vcc
	s_cbranch_execz .LBB0_1383
	v_mov_b32_e32 v10, v246
	v_lshrrev_b32_e32 v9, 30, v8
	v_and_b32_e32 v8, 0x3fffffff, v8
	s_movk_i32 s37, 0x4800
	v_mad_u32_u24 v8, v9, s37, v8
	v_mov_b32_e32 v9, v0
	v_lshlrev_b64 v[8:9], 11, v[8:9]
	v_lshl_add_u64 v[8:9], s[16:17], 0, v[8:9]
	v_lshl_add_u64 v[8:9], v[8:9], 0, v[2:3]
	v_pk_mul_f32 v[12:13], v[96:97], v[10:11] op_sel_hi:[1,0]
	v_pk_mul_f32 v[14:15], v[94:95], v[10:11] op_sel_hi:[1,0]
	v_pk_mul_f32 v[16:17], v[92:93], v[10:11] op_sel_hi:[1,0]
	v_pk_mul_f32 v[18:19], v[90:91], v[10:11] op_sel_hi:[1,0]
	v_med3_f32 v11, v14, s83, v238
	v_med3_f32 v14, v15, s83, v238
	v_med3_f32 v15, v12, s83, v238
	v_mov_b32_e32 v12, v0
	v_cvt_pk_fp8_f32 v12, v11, v14
	v_med3_f32 v13, v13, s83, v238
	v_med3_f32 v11, v18, s83, v238
	v_med3_f32 v14, v19, s83, v238
	v_cvt_pk_fp8_f32 v12, v15, v13 op_sel:[0,0,1]
	v_mov_b32_e32 v13, v0
	v_cvt_pk_fp8_f32 v13, v11, v14
	v_med3_f32 v15, v16, s83, v238
	v_med3_f32 v16, v17, s83, v238
	v_cvt_pk_fp8_f32 v13, v15, v16 op_sel:[0,0,1]
	v_pk_mul_f32 v[14:15], v[86:87], v[10:11] op_sel_hi:[1,0]
	v_pk_mul_f32 v[16:17], v[84:85], v[10:11] op_sel_hi:[1,0]
	v_med3_f32 v14, v14, s83, v238
	global_store_dwordx2 v[8:9], v[12:13], off
	v_pk_mul_f32 v[12:13], v[88:89], v[10:11] op_sel_hi:[1,0]
	v_med3_f32 v15, v15, s83, v238
	v_med3_f32 v18, v12, s83, v238
	v_mov_b32_e32 v12, v0
	v_cvt_pk_fp8_f32 v12, v14, v15
	v_pk_mul_f32 v[10:11], v[82:83], v[10:11] op_sel_hi:[1,0]
	v_med3_f32 v13, v13, s83, v238
	v_med3_f32 v10, v10, s83, v238
	v_cvt_pk_fp8_f32 v12, v18, v13 op_sel:[0,0,1]
	v_med3_f32 v11, v11, s83, v238
	v_mov_b32_e32 v13, v0
	v_cvt_pk_fp8_f32 v13, v10, v11
	v_med3_f32 v14, v16, s83, v238
	v_med3_f32 v15, v17, s83, v238
	v_cvt_pk_fp8_f32 v13, v14, v15 op_sel:[0,0,1]
	global_store_dwordx2 v[8:9], v[12:13], off offset:128
;     __device__ __forceinline__ void operator()(const f32x4 (&acc)[2][2][4][2], const Unit& u, int wr, int wc, int fr, int fq) const {
;         const int row0 = u.pm * BM + wr * 64 + fr, col0 = (u.pn & 7) * BM + wc * 32 + 8 * fq;
; #pragma unroll
;         for (int ai = 0; ai < 2; ++ai)
; #pragma unroll
;             for (int m = 0; m < 4; ++m) { asm volatile("" ::: "memory"); const int row = row0 + ai * HALF + m * 16; const int tk = rowtok[row]; const float w = roww[row];
;                 if (tk >= 0) { unsigned char* rowp = Y2 + ((size_t)(tk >> 30) * TT + (size_t)(tk & 0x3fffffff)) * D + col0;
; #pragma unroll
;                     for (int bj = 0; bj < 2; ++bj) { const f32x4 v0 = acc[ai][bj][m][0] * w, v1 = acc[ai][bj][m][1] * w;
;                         u32x2 o; o.x = pk4_f8(v0[0], v0[1], v0[2], v0[3]); o.y = pk4_f8(v1[0], v1[1], v1[2], v1[3]);
;                         *(u32x2*)(rowp + bj * HALF) = o; } } }
;     }
.LBB0_1383:
	s_or_b64 exec, exec, s[34:35]
	v_mov_b32_e32 v8, v225
	v_cmp_lt_i32_e32 vcc, -1, v8
	s_and_saveexec_b64 s[34:35], vcc
	s_cbranch_execz .LBB0_1385
	v_mov_b32_e32 v10, v247
	v_lshrrev_b32_e32 v9, 30, v8
	v_and_b32_e32 v8, 0x3fffffff, v8
	s_movk_i32 s37, 0x4800
	v_mad_u32_u24 v8, v9, s37, v8
	v_mov_b32_e32 v9, v0
	v_lshlrev_b64 v[8:9], 11, v[8:9]
	v_lshl_add_u64 v[8:9], s[16:17], 0, v[8:9]
	v_lshl_add_u64 v[8:9], v[8:9], 0, v[2:3]
	v_pk_mul_f32 v[12:13], v[80:81], v[10:11] op_sel_hi:[1,0]
	v_pk_mul_f32 v[14:15], v[78:79], v[10:11] op_sel_hi:[1,0]
	v_pk_mul_f32 v[16:17], v[76:77], v[10:11] op_sel_hi:[1,0]
	v_pk_mul_f32 v[18:19], v[74:75], v[10:11] op_sel_hi:[1,0]
	v_med3_f32 v11, v14, s83, v238
	v_med3_f32 v14, v15, s83, v238
	v_med3_f32 v15, v12, s83, v238
	v_mov_b32_e32 v12, v0
	v_cvt_pk_fp8_f32 v12, v11, v14
	v_med3_f32 v13, v13, s83, v238
	v_med3_f32 v11, v18, s83, v238
	v_med3_f32 v14, v19, s83, v238
	v_cvt_pk_fp8_f32 v12, v15, v13 op_sel:[0,0,1]
	v_mov_b32_e32 v13, v0
	v_cvt_pk_fp8_f32 v13, v11, v14
	v_med3_f32 v15, v16, s83, v238
	v_med3_f32 v16, v17, s83, v238
	v_cvt_pk_fp8_f32 v13, v15, v16 op_sel:[0,0,1]
	v_pk_mul_f32 v[14:15], v[70:71], v[10:11] op_sel_hi:[1,0]
	v_pk_mul_f32 v[16:17], v[68:69], v[10:11] op_sel_hi:[1,0]
	v_med3_f32 v14, v14, s83, v238
	global_store_dwordx2 v[8:9], v[12:13], off
	v_pk_mul_f32 v[12:13], v[72:73], v[10:11] op_sel_hi:[1,0]
	v_med3_f32 v15, v15, s83, v238
	v_med3_f32 v18, v12, s83, v238
	v_mov_b32_e32 v12, v0
	v_cvt_pk_fp8_f32 v12, v14, v15
	v_pk_mul_f32 v[10:11], v[66:67], v[10:11] op_sel_hi:[1,0]
	v_med3_f32 v13, v13, s83, v238
	v_med3_f32 v10, v10, s83, v238
	v_cvt_pk_fp8_f32 v12, v18, v13 op_sel:[0,0,1]
	v_med3_f32 v11, v11, s83, v238
	v_mov_b32_e32 v13, v0
	v_cvt_pk_fp8_f32 v13, v10, v11
	v_med3_f32 v14, v16, s83, v238
	v_med3_f32 v15, v17, s83, v238
	v_cvt_pk_fp8_f32 v13, v14, v15 op_sel:[0,0,1]
	global_store_dwordx2 v[8:9], v[12:13], off offset:128
.LBB0_1385:
	s_or_b64 exec, exec, s[34:35]
	v_mov_b32_e32 v8, v228
	v_cmp_lt_i32_e32 vcc, -1, v8
	s_and_saveexec_b64 s[34:35], vcc
	s_cbranch_execz .LBB0_1387
	v_mov_b32_e32 v10, v248
	v_lshrrev_b32_e32 v9, 30, v8
	v_and_b32_e32 v8, 0x3fffffff, v8
	s_movk_i32 s37, 0x4800
	v_mad_u32_u24 v8, v9, s37, v8
	v_mov_b32_e32 v9, v0
	v_lshlrev_b64 v[8:9], 11, v[8:9]
	v_lshl_add_u64 v[8:9], s[16:17], 0, v[8:9]
	v_lshl_add_u64 v[8:9], v[8:9], 0, v[2:3]
	v_pk_mul_f32 v[12:13], v[64:65], v[10:11] op_sel_hi:[1,0]
	v_pk_mul_f32 v[14:15], v[62:63], v[10:11] op_sel_hi:[1,0]
	v_pk_mul_f32 v[16:17], v[60:61], v[10:11] op_sel_hi:[1,0]
	v_pk_mul_f32 v[18:19], v[58:59], v[10:11] op_sel_hi:[1,0]
	v_med3_f32 v11, v14, s83, v238
	v_med3_f32 v14, v15, s83, v238
	v_med3_f32 v15, v12, s83, v238
	v_mov_b32_e32 v12, v0
	v_cvt_pk_fp8_f32 v12, v11, v14
	v_med3_f32 v13, v13, s83, v238
	v_med3_f32 v11, v18, s83, v238
	v_med3_f32 v14, v19, s83, v238
	v_cvt_pk_fp8_f32 v12, v15, v13 op_sel:[0,0,1]
	v_mov_b32_e32 v13, v0
	v_cvt_pk_fp8_f32 v13, v11, v14
	v_med3_f32 v15, v16, s83, v238
	v_med3_f32 v16, v17, s83, v238
	v_cvt_pk_fp8_f32 v13, v15, v16 op_sel:[0,0,1]
	v_pk_mul_f32 v[14:15], v[54:55], v[10:11] op_sel_hi:[1,0]
	v_pk_mul_f32 v[16:17], v[52:53], v[10:11] op_sel_hi:[1,0]
	v_med3_f32 v14, v14, s83, v238
	global_store_dwordx2 v[8:9], v[12:13], off
	v_pk_mul_f32 v[12:13], v[56:57], v[10:11] op_sel_hi:[1,0]
	v_med3_f32 v15, v15, s83, v238
	v_med3_f32 v18, v12, s83, v238
	v_mov_b32_e32 v12, v0
	v_cvt_pk_fp8_f32 v12, v14, v15
	v_pk_mul_f32 v[10:11], v[50:51], v[10:11] op_sel_hi:[1,0]
	v_med3_f32 v13, v13, s83, v238
	v_med3_f32 v10, v10, s83, v238
	v_cvt_pk_fp8_f32 v12, v18, v13 op_sel:[0,0,1]
	v_med3_f32 v11, v11, s83, v238
	v_mov_b32_e32 v13, v0
	v_cvt_pk_fp8_f32 v13, v10, v11
	v_med3_f32 v14, v16, s83, v238
	v_med3_f32 v15, v17, s83, v238
	v_cvt_pk_fp8_f32 v13, v14, v15 op_sel:[0,0,1]
	global_store_dwordx2 v[8:9], v[12:13], off offset:128
.LBB0_1387:
	s_or_b64 exec, exec, s[34:35]
	v_mov_b32_e32 v6, v229
	v_cmp_lt_i32_e32 vcc, -1, v6
	s_and_saveexec_b64 s[34:35], vcc
	s_cbranch_execz .LBB0_1389
	v_mov_b32_e32 v4, v249
	v_lshrrev_b32_e32 v5, 30, v6
	v_and_b32_e32 v6, 0x3fffffff, v6
	s_movk_i32 s37, 0x4800
	v_mad_u32_u24 v6, v5, s37, v6
	v_mov_b32_e32 v7, v0
	v_lshlrev_b64 v[6:7], 11, v[6:7]
	v_lshl_add_u64 v[6:7], s[16:17], 0, v[6:7]
	v_lshl_add_u64 v[2:3], v[6:7], 0, v[2:3]
	v_pk_mul_f32 v[6:7], v[48:49], v[4:5] op_sel_hi:[1,0]
	v_pk_mul_f32 v[8:9], v[46:47], v[4:5] op_sel_hi:[1,0]
	v_pk_mul_f32 v[10:11], v[44:45], v[4:5] op_sel_hi:[1,0]
	v_pk_mul_f32 v[12:13], v[42:43], v[4:5] op_sel_hi:[1,0]
	v_med3_f32 v5, v8, s83, v238
	v_med3_f32 v8, v9, s83, v238
	v_med3_f32 v9, v6, s83, v238
	v_mov_b32_e32 v6, v0
	v_cvt_pk_fp8_f32 v6, v5, v8
	v_med3_f32 v7, v7, s83, v238
	v_med3_f32 v5, v12, s83, v238
	v_med3_f32 v8, v13, s83, v238
	v_cvt_pk_fp8_f32 v6, v9, v7 op_sel:[0,0,1]
	v_mov_b32_e32 v7, v0
	v_cvt_pk_fp8_f32 v7, v5, v8
	v_med3_f32 v9, v10, s83, v238
	v_med3_f32 v10, v11, s83, v238
	v_cvt_pk_fp8_f32 v7, v9, v10 op_sel:[0,0,1]
	v_pk_mul_f32 v[8:9], v[38:39], v[4:5] op_sel_hi:[1,0]
	v_pk_mul_f32 v[10:11], v[36:37], v[4:5] op_sel_hi:[1,0]
	v_med3_f32 v8, v8, s83, v238
	global_store_dwordx2 v[2:3], v[6:7], off
	v_pk_mul_f32 v[6:7], v[40:41], v[4:5] op_sel_hi:[1,0]
	v_med3_f32 v9, v9, s83, v238
	v_med3_f32 v12, v6, s83, v238
	v_mov_b32_e32 v6, v0
	v_cvt_pk_fp8_f32 v6, v8, v9
	v_pk_mul_f32 v[4:5], v[34:35], v[4:5] op_sel_hi:[1,0]
	v_med3_f32 v7, v7, s83, v238
	v_med3_f32 v4, v4, s83, v238
	v_cvt_pk_fp8_f32 v6, v12, v7 op_sel:[0,0,1]
	v_med3_f32 v5, v5, s83, v238
	v_mov_b32_e32 v7, v0
	v_cvt_pk_fp8_f32 v7, v4, v5
	v_med3_f32 v8, v10, s83, v238
	v_med3_f32 v9, v11, s83, v238
	v_cvt_pk_fp8_f32 v7, v8, v9 op_sel:[0,0,1]
	global_store_dwordx2 v[2:3], v[6:7], off offset:128
